# hand-written layer1 as well (self x rows loaded in set-B tail, exec-masked padded gathers, sc1 stores) + hand layer2 + sort1 conv delay
# speedup vs baseline: 1.3050x; 1.0185x over previous
_Z12layer_kernelILb1ELi128EEvPKfPKDF16_PKhS3_PK15HIP_vector_typeIiLj4EEPKtPKiS3_S1_PvPhPDF16_:
	s_load_dwordx8 s[8:15], s[0:1], 0x0
	s_load_dwordx8 s[16:23], s[0:1], 0x20
	s_load_dwordx8 s[24:31], s[0:1], 0x40
	v_lshrrev_b32_e32 v94, 6, v0
	v_and_b32_e32 v1, 63, v0
	v_lshlrev_b32_e32 v95, 4, v0
	v_readfirstlane_b32 s3, v94
	s_and_b32 s4, s2, 7
	s_lshr_b32 s5, s2, 3
	s_lshl_b32 s7, s3, 5
	s_add_u32 s5, s5, s7
	s_movk_i32 s7, 0x185
	s_cmp_eq_u32 s4, 3
	s_cselect_b32 s7, s7, 0x180
	s_movk_i32 s58, 0x190
	s_cmp_lt_u32 s4, 3
	s_cselect_b32 s7, s58, s7
	s_lshr_b32 s6, s5, 4
	s_lshl_b32 s6, s6, 3
	s_add_u32 s6, s6, s4
	s_lshl_b32 s6, s6, 4
	s_and_b32 s58, s5, 15
	s_add_u32 s6, s6, s58
	v_lshrrev_b32_e32 v96, 5, v0
	v_and_b32_e32 v97, 31, v0
	v_and_b32_e32 v98, 15, v96
	v_xor_b32_e32 v97, v97, v98
	v_lshlrev_b32_e32 v97, 4, v97
	v_lshl_or_b32 v96, v96, 9, v97
	v_add_u32_e32 v98, 0x4000, v95
	v_add_u32_e32 v99, 0x8000, v95
	v_add_u32_e32 v100, 0xc000, v95
	s_cmp_lt_u32 s5, s7
	s_cbranch_scc1 .Lg1_active
	s_waitcnt lgkmcnt(0)
	global_load_dwordx4 v[2:5], v95, s[22:23]
	global_load_dwordx4 v[6:9], v98, s[22:23]
	global_load_dwordx4 v[10:13], v99, s[22:23]
	global_load_dwordx4 v[14:17], v100, s[22:23]
	s_waitcnt vmcnt(0)
	ds_write_b128 v96, v[2:5]
	ds_write_b128 v96, v[6:9] offset:16384
	ds_write_b128 v96, v[10:13] offset:32768
	ds_write_b128 v96, v[14:17] offset:49152
	s_waitcnt lgkmcnt(0)
	s_barrier
	s_endpgm
.Lg1_active:
	s_mov_b32 s60, 0x00ff00ff
	s_mov_b32 s61, 0x0c030c01
	v_lshrrev_b32_e32 v107, 3, v1
	v_and_b32_e32 v108, 7, v1
	v_and_b32_e32 v105, 15, v1
	v_lshrrev_b32_e32 v106, 4, v1
	s_bfe_u32 s36, s3, 0x10002
	s_lshl_b32 s58, s36, 3
	s_xor_b32 s59, s58, 8
	v_or_b32_e32 v102, s58, v107
	v_or_b32_e32 v103, s59, v107
	v_lshlrev_b32_e32 v89, 4, v108
	v_and_b32_e32 v90, 56, v1
	v_lshlrev_b32_e32 v90, 2, v90
	s_waitcnt lgkmcnt(0)
	s_lshl_b32 s58, s6, 8
	s_add_u32 s32, s16, s58
	s_addc_u32 s33, s17, 0
	s_lshl_b32 s58, s6, 10
	s_add_u32 s34, s18, s58
	s_addc_u32 s35, s19, 0
	v_lshlrev_b32_e32 v109, 4, v105
	global_load_dword v104, v109, s[32:33] offset:8
	v_lshlrev_b32_e32 v110, 4, v102
	global_load_dwordx2 v[68:69], v110, s[32:33]
	v_lshlrev_b32_e32 v111, 4, v103
	global_load_dwordx2 v[70:71], v111, s[32:33]
	v_lshlrev_b32_e32 v101, 2, v108
	v_lshl_or_b32 v110, v102, 6, v101
	global_load_dword v60, v110, s[34:35]
	global_load_dword v61, v110, s[34:35] offset:32
	v_lshl_or_b32 v111, v103, 6, v101
	global_load_dword v62, v111, s[34:35]
	global_load_dword v63, v111, s[34:35] offset:32
	global_load_dwordx4 v[2:5], v95, s[22:23]
	global_load_dwordx4 v[6:9], v98, s[22:23]
	global_load_dwordx4 v[10:13], v99, s[22:23]
	global_load_dwordx4 v[14:17], v100, s[22:23]
	v_and_b32_e32 v101, 0x7f, v0
	v_lshlrev_b32_e32 v101, 2, v101
	global_load_dword v19, v101, s[24:25]
	s_mul_i32 s48, s3, 0x1100
	s_add_u32 s48, s48, 0x10200
	v_mul_u32_u24_e32 v91, 0x110, v102
	v_lshl_add_u32 v91, v108, 5, v91
	v_add_u32_e32 v91, s48, v91
	v_mul_u32_u24_e32 v92, 0x110, v103
	v_lshl_add_u32 v92, v108, 5, v92
	v_add_u32_e32 v92, s48, v92
	s_waitcnt vmcnt(5)
	v_readlane_b32 s49, v69, 0
	v_readlane_b32 s50, v69, 8
	v_readlane_b32 s51, v69, 16
	v_readlane_b32 s52, v69, 24
	v_readlane_b32 s53, v69, 32
	v_readlane_b32 s54, v69, 40
	v_readlane_b32 s55, v69, 48
	v_readlane_b32 s56, v69, 56
	s_max_i32 s37, s49, s50
	s_max_i32 s37, s37, s51
	s_max_i32 s37, s37, s52
	s_max_i32 s37, s37, s53
	s_max_i32 s37, s37, s54
	s_max_i32 s37, s37, s55
	s_max_i32 s37, s37, s56
	v_readlane_b32 s49, v71, 0
	v_readlane_b32 s50, v71, 8
	v_readlane_b32 s51, v71, 16
	v_readlane_b32 s52, v71, 24
	v_readlane_b32 s53, v71, 32
	v_readlane_b32 s54, v71, 40
	v_readlane_b32 s55, v71, 48
	v_readlane_b32 s56, v71, 56
	s_max_i32 s38, s49, s50
	s_max_i32 s38, s38, s51
	s_max_i32 s38, s38, s52
	s_max_i32 s38, s38, s53
	s_max_i32 s38, s38, s54
	s_max_i32 s38, s38, s55
	s_max_i32 s38, s38, s56
	v_and_b32_e32 v103, 0xffff, v60
	v_lshlrev_b32_e32 v103, 1, v103
	global_load_ushort v52, v103, s[14:15]
	v_lshrrev_b32_e32 v109, 16, v60
	v_lshlrev_b32_e32 v109, 1, v109
	global_load_ushort v53, v109, s[14:15]
	v_and_b32_e32 v103, 0xffff, v61
	v_lshlrev_b32_e32 v103, 1, v103
	global_load_ushort v54, v103, s[14:15]
	v_lshrrev_b32_e32 v109, 16, v61
	v_lshlrev_b32_e32 v109, 1, v109
	global_load_ushort v55, v109, s[14:15]
	v_and_b32_e32 v103, 0xffff, v62
	v_lshlrev_b32_e32 v103, 1, v103
	global_load_ushort v56, v103, s[14:15]
	v_lshrrev_b32_e32 v109, 16, v62
	v_lshlrev_b32_e32 v109, 1, v109
	global_load_ushort v57, v109, s[14:15]
	v_and_b32_e32 v103, 0xffff, v63
	v_lshlrev_b32_e32 v103, 1, v103
	global_load_ushort v58, v103, s[14:15]
	v_lshrrev_b32_e32 v109, 16, v63
	v_lshlrev_b32_e32 v109, 1, v109
	global_load_ushort v59, v109, s[14:15]
	v_lshlrev_b32_e32 v103, 9, v104
	v_lshl_or_b32 v103, v106, 5, v103
	s_waitcnt vmcnt(8)
	ds_write_b128 v96, v[2:5]
	ds_write_b128 v96, v[6:9] offset:16384
	ds_write_b128 v96, v[10:13] offset:32768
	ds_write_b128 v96, v[14:17] offset:49152
	v_add_u32_e32 v101, 0x10000, v101
	ds_write_b32 v101, v19
	s_waitcnt lgkmcnt(0)
	s_barrier
	s_mov_b32 s39, 0
	s_waitcnt vmcnt(0)
	v_lshl_or_b32 v64, v53, 16, v52
	v_lshl_or_b32 v65, v55, 16, v54
	v_lshl_or_b32 v66, v57, 16, v56
	v_lshl_or_b32 v67, v59, 16, v58

.Lg1_sel_done:
	s_min_i32 s40, s41, 32
	s_add_i32 s40, s40, 3
	s_and_b32 s40, s40, 0x3c
	s_max_i32 s40, s40, 8
	v_mov_b32_e32 v2, 0
	v_mov_b32_e32 v3, 0
	v_mov_b32_e32 v4, 0
	v_mov_b32_e32 v5, 0
	v_mov_b32_e32 v6, 0
	v_mov_b32_e32 v7, 0
	v_mov_b32_e32 v8, 0
	v_mov_b32_e32 v9, 0
	v_mov_b32_e32 v10, 0
	v_mov_b32_e32 v11, 0
	v_mov_b32_e32 v12, 0
	v_mov_b32_e32 v13, 0
	v_mov_b32_e32 v14, 0
	v_mov_b32_e32 v15, 0
	v_mov_b32_e32 v16, 0
	v_mov_b32_e32 v17, 0
	v_mov_b32_e32 v18, 0
	s_waitcnt lgkmcnt(0)
	ds_bpermute_b32 v94, v90, v73 offset:0
	ds_bpermute_b32 v98, v90, v75 offset:0
	ds_bpermute_b32 v95, v90, v73 offset:4
	ds_bpermute_b32 v99, v90, v75 offset:4
	ds_bpermute_b32 v96, v90, v73 offset:8
	ds_bpermute_b32 v100, v90, v75 offset:8
	ds_bpermute_b32 v97, v90, v73 offset:12
	ds_bpermute_b32 v101, v90, v75 offset:12
	ds_bpermute_b32 v79, v90, v73 offset:16
	ds_bpermute_b32 v81, v90, v75 offset:16
	s_waitcnt lgkmcnt(2)
	v_and_b32_e32 v84, 0xffff, v94
	v_lshl_or_b32 v83, v84, 7, v89
	v_cmp_lt_i32_e32 vcc, 0, v78
	s_mov_b64 exec, vcc
	global_load_dwordx4 v[20:23], v83, s[12:13]
	s_mov_b64 exec, -1
	v_cvt_f32_f16_e32 v52, v98
	v_lshrrev_b32_e32 v84, 16, v94
	v_lshl_or_b32 v83, v84, 7, v89
	v_cmp_lt_i32_e32 vcc, 1, v78
	s_mov_b64 exec, vcc
	global_load_dwordx4 v[24:27], v83, s[12:13]
	s_mov_b64 exec, -1
	v_cvt_f32_f16_sdwa v53, v98 dst_sel:DWORD dst_unused:UNUSED_PAD src0_sel:WORD_1
	v_and_b32_e32 v84, 0xffff, v95
	v_lshl_or_b32 v83, v84, 7, v89
	v_cmp_lt_i32_e32 vcc, 2, v78
	s_mov_b64 exec, vcc
	global_load_dwordx4 v[28:31], v83, s[12:13]
	s_mov_b64 exec, -1
	v_cvt_f32_f16_e32 v54, v99
	v_lshrrev_b32_e32 v84, 16, v95
	v_lshl_or_b32 v83, v84, 7, v89
	v_cmp_lt_i32_e32 vcc, 3, v78
	s_mov_b64 exec, vcc
	global_load_dwordx4 v[32:35], v83, s[12:13]
	s_mov_b64 exec, -1
	v_cvt_f32_f16_sdwa v55, v99 dst_sel:DWORD dst_unused:UNUSED_PAD src0_sel:WORD_1
	v_and_b32_e32 v84, 0xffff, v96
	v_lshl_or_b32 v83, v84, 7, v89
	v_cmp_lt_i32_e32 vcc, 4, v78
	s_mov_b64 exec, vcc
	global_load_dwordx4 v[36:39], v83, s[12:13]
	s_mov_b64 exec, -1
	v_cvt_f32_f16_e32 v56, v100
	v_lshrrev_b32_e32 v84, 16, v96
	v_lshl_or_b32 v83, v84, 7, v89
	v_cmp_lt_i32_e32 vcc, 5, v78
	s_mov_b64 exec, vcc
	global_load_dwordx4 v[40:43], v83, s[12:13]
	s_mov_b64 exec, -1
	v_cvt_f32_f16_sdwa v57, v100 dst_sel:DWORD dst_unused:UNUSED_PAD src0_sel:WORD_1
	v_and_b32_e32 v84, 0xffff, v97
	v_lshl_or_b32 v83, v84, 7, v89
	v_cmp_lt_i32_e32 vcc, 6, v78
	s_mov_b64 exec, vcc
	global_load_dwordx4 v[44:47], v83, s[12:13]
	s_mov_b64 exec, -1
	v_cvt_f32_f16_e32 v58, v101
	v_lshrrev_b32_e32 v84, 16, v97
	v_lshl_or_b32 v83, v84, 7, v89
	v_cmp_lt_i32_e32 vcc, 7, v78
	s_mov_b64 exec, vcc
	global_load_dwordx4 v[48:51], v83, s[12:13]
	s_mov_b64 exec, -1
	v_cvt_f32_f16_sdwa v59, v101 dst_sel:DWORD dst_unused:UNUSED_PAD src0_sel:WORD_1
	s_cmp_le_u32 s40, 8
	s_cbranch_scc1 .Lg1_tail0
	s_waitcnt lgkmcnt(0)
	ds_bpermute_b32 v80, v90, v73 offset:20
	ds_bpermute_b32 v82, v90, v75 offset:20
	s_waitcnt vmcnt(7)
	v_cvt_f32_ubyte0_e32 v85, v20
	v_cvt_f32_ubyte1_e32 v86, v20
	v_cvt_f32_ubyte2_e32 v87, v20
	v_cvt_f32_ubyte3_e32 v88, v20
	v_fmac_f32_e32 v2, v85, v52
	v_fmac_f32_e32 v3, v86, v52
	v_fmac_f32_e32 v4, v87, v52
	v_fmac_f32_e32 v5, v88, v52
	v_cvt_f32_ubyte0_e32 v85, v21
	v_cvt_f32_ubyte1_e32 v86, v21
	v_cvt_f32_ubyte2_e32 v87, v21
	v_cvt_f32_ubyte3_e32 v88, v21
	v_fmac_f32_e32 v6, v85, v52
	v_fmac_f32_e32 v7, v86, v52
	v_fmac_f32_e32 v8, v87, v52
	v_fmac_f32_e32 v9, v88, v52
	v_cvt_f32_ubyte0_e32 v85, v22
	v_cvt_f32_ubyte1_e32 v86, v22
	v_cvt_f32_ubyte2_e32 v87, v22
	v_cvt_f32_ubyte3_e32 v88, v22
	v_fmac_f32_e32 v10, v85, v52
	v_fmac_f32_e32 v11, v86, v52
	v_fmac_f32_e32 v12, v87, v52
	v_fmac_f32_e32 v13, v88, v52
	v_cvt_f32_ubyte0_e32 v85, v23
	v_cvt_f32_ubyte1_e32 v86, v23
	v_cvt_f32_ubyte2_e32 v87, v23
	v_cvt_f32_ubyte3_e32 v88, v23
	v_fmac_f32_e32 v14, v85, v52
	v_fmac_f32_e32 v15, v86, v52
	v_fmac_f32_e32 v16, v87, v52
	v_fmac_f32_e32 v17, v88, v52
	v_add_f32_e32 v18, v18, v52
	v_and_b32_e32 v84, 0xffff, v79
	v_lshl_or_b32 v83, v84, 7, v89
	v_cmp_lt_i32_e32 vcc, 8, v78
	s_mov_b64 exec, vcc
	global_load_dwordx4 v[20:23], v83, s[12:13]
	s_mov_b64 exec, -1
	v_cvt_f32_f16_e32 v52, v81
	s_waitcnt vmcnt(7)
	v_cvt_f32_ubyte0_e32 v85, v24
	v_cvt_f32_ubyte1_e32 v86, v24
	v_cvt_f32_ubyte2_e32 v87, v24
	v_cvt_f32_ubyte3_e32 v88, v24
	v_fmac_f32_e32 v2, v85, v53
	v_fmac_f32_e32 v3, v86, v53
	v_fmac_f32_e32 v4, v87, v53
	v_fmac_f32_e32 v5, v88, v53
	v_cvt_f32_ubyte0_e32 v85, v25
	v_cvt_f32_ubyte1_e32 v86, v25
	v_cvt_f32_ubyte2_e32 v87, v25
	v_cvt_f32_ubyte3_e32 v88, v25
	v_fmac_f32_e32 v6, v85, v53
	v_fmac_f32_e32 v7, v86, v53
	v_fmac_f32_e32 v8, v87, v53
	v_fmac_f32_e32 v9, v88, v53
	v_cvt_f32_ubyte0_e32 v85, v26
	v_cvt_f32_ubyte1_e32 v86, v26
	v_cvt_f32_ubyte2_e32 v87, v26
	v_cvt_f32_ubyte3_e32 v88, v26
	v_fmac_f32_e32 v10, v85, v53
	v_fmac_f32_e32 v11, v86, v53
	v_fmac_f32_e32 v12, v87, v53
	v_fmac_f32_e32 v13, v88, v53
	v_cvt_f32_ubyte0_e32 v85, v27
	v_cvt_f32_ubyte1_e32 v86, v27
	v_cvt_f32_ubyte2_e32 v87, v27
	v_cvt_f32_ubyte3_e32 v88, v27
	v_fmac_f32_e32 v14, v85, v53
	v_fmac_f32_e32 v15, v86, v53
	v_fmac_f32_e32 v16, v87, v53
	v_fmac_f32_e32 v17, v88, v53
	v_add_f32_e32 v18, v18, v53
	v_lshrrev_b32_e32 v84, 16, v79
	v_lshl_or_b32 v83, v84, 7, v89
	v_cmp_lt_i32_e32 vcc, 9, v78
	s_mov_b64 exec, vcc
	global_load_dwordx4 v[24:27], v83, s[12:13]
	s_mov_b64 exec, -1
	v_cvt_f32_f16_sdwa v53, v81 dst_sel:DWORD dst_unused:UNUSED_PAD src0_sel:WORD_1
	s_waitcnt lgkmcnt(0)
	ds_bpermute_b32 v79, v90, v73 offset:24
	ds_bpermute_b32 v81, v90, v75 offset:24
	s_waitcnt vmcnt(7)
	v_cvt_f32_ubyte0_e32 v85, v28
	v_cvt_f32_ubyte1_e32 v86, v28
	v_cvt_f32_ubyte2_e32 v87, v28
	v_cvt_f32_ubyte3_e32 v88, v28
	v_fmac_f32_e32 v2, v85, v54
	v_fmac_f32_e32 v3, v86, v54
	v_fmac_f32_e32 v4, v87, v54
	v_fmac_f32_e32 v5, v88, v54
	v_cvt_f32_ubyte0_e32 v85, v29
	v_cvt_f32_ubyte1_e32 v86, v29
	v_cvt_f32_ubyte2_e32 v87, v29
	v_cvt_f32_ubyte3_e32 v88, v29
	v_fmac_f32_e32 v6, v85, v54
	v_fmac_f32_e32 v7, v86, v54
	v_fmac_f32_e32 v8, v87, v54
	v_fmac_f32_e32 v9, v88, v54
	v_cvt_f32_ubyte0_e32 v85, v30
	v_cvt_f32_ubyte1_e32 v86, v30
	v_cvt_f32_ubyte2_e32 v87, v30
	v_cvt_f32_ubyte3_e32 v88, v30
	v_fmac_f32_e32 v10, v85, v54
	v_fmac_f32_e32 v11, v86, v54
	v_fmac_f32_e32 v12, v87, v54
	v_fmac_f32_e32 v13, v88, v54
	v_cvt_f32_ubyte0_e32 v85, v31
	v_cvt_f32_ubyte1_e32 v86, v31
	v_cvt_f32_ubyte2_e32 v87, v31
	v_cvt_f32_ubyte3_e32 v88, v31
	v_fmac_f32_e32 v14, v85, v54
	v_fmac_f32_e32 v15, v86, v54
	v_fmac_f32_e32 v16, v87, v54
	v_fmac_f32_e32 v17, v88, v54
	v_add_f32_e32 v18, v18, v54
	v_and_b32_e32 v84, 0xffff, v80
	v_lshl_or_b32 v83, v84, 7, v89
	v_cmp_lt_i32_e32 vcc, 10, v78
	s_mov_b64 exec, vcc
	global_load_dwordx4 v[28:31], v83, s[12:13]
	s_mov_b64 exec, -1
	v_cvt_f32_f16_e32 v54, v82
	s_waitcnt vmcnt(7)
	v_cvt_f32_ubyte0_e32 v85, v32
	v_cvt_f32_ubyte1_e32 v86, v32
	v_cvt_f32_ubyte2_e32 v87, v32
	v_cvt_f32_ubyte3_e32 v88, v32
	v_fmac_f32_e32 v2, v85, v55
	v_fmac_f32_e32 v3, v86, v55
	v_fmac_f32_e32 v4, v87, v55
	v_fmac_f32_e32 v5, v88, v55
	v_cvt_f32_ubyte0_e32 v85, v33
	v_cvt_f32_ubyte1_e32 v86, v33
	v_cvt_f32_ubyte2_e32 v87, v33
	v_cvt_f32_ubyte3_e32 v88, v33
	v_fmac_f32_e32 v6, v85, v55
	v_fmac_f32_e32 v7, v86, v55
	v_fmac_f32_e32 v8, v87, v55
	v_fmac_f32_e32 v9, v88, v55
	v_cvt_f32_ubyte0_e32 v85, v34
	v_cvt_f32_ubyte1_e32 v86, v34
	v_cvt_f32_ubyte2_e32 v87, v34
	v_cvt_f32_ubyte3_e32 v88, v34
	v_fmac_f32_e32 v10, v85, v55
	v_fmac_f32_e32 v11, v86, v55
	v_fmac_f32_e32 v12, v87, v55
	v_fmac_f32_e32 v13, v88, v55
	v_cvt_f32_ubyte0_e32 v85, v35
	v_cvt_f32_ubyte1_e32 v86, v35
	v_cvt_f32_ubyte2_e32 v87, v35
	v_cvt_f32_ubyte3_e32 v88, v35
	v_fmac_f32_e32 v14, v85, v55
	v_fmac_f32_e32 v15, v86, v55
	v_fmac_f32_e32 v16, v87, v55
	v_fmac_f32_e32 v17, v88, v55
	v_add_f32_e32 v18, v18, v55
	v_lshrrev_b32_e32 v84, 16, v80
	v_lshl_or_b32 v83, v84, 7, v89
	v_cmp_lt_i32_e32 vcc, 11, v78
	s_mov_b64 exec, vcc
	global_load_dwordx4 v[32:35], v83, s[12:13]
	s_mov_b64 exec, -1
	v_cvt_f32_f16_sdwa v55, v82 dst_sel:DWORD dst_unused:UNUSED_PAD src0_sel:WORD_1
	s_cmp_le_u32 s40, 12
	s_cbranch_scc1 .Lg1_tail4
	s_waitcnt lgkmcnt(0)
	ds_bpermute_b32 v80, v90, v73 offset:28
	ds_bpermute_b32 v82, v90, v75 offset:28
	s_waitcnt vmcnt(7)
	v_cvt_f32_ubyte0_e32 v85, v36
	v_cvt_f32_ubyte1_e32 v86, v36
	v_cvt_f32_ubyte2_e32 v87, v36
	v_cvt_f32_ubyte3_e32 v88, v36
	v_fmac_f32_e32 v2, v85, v56
	v_fmac_f32_e32 v3, v86, v56
	v_fmac_f32_e32 v4, v87, v56
	v_fmac_f32_e32 v5, v88, v56
	v_cvt_f32_ubyte0_e32 v85, v37
	v_cvt_f32_ubyte1_e32 v86, v37
	v_cvt_f32_ubyte2_e32 v87, v37
	v_cvt_f32_ubyte3_e32 v88, v37
	v_fmac_f32_e32 v6, v85, v56
	v_fmac_f32_e32 v7, v86, v56
	v_fmac_f32_e32 v8, v87, v56
	v_fmac_f32_e32 v9, v88, v56
	v_cvt_f32_ubyte0_e32 v85, v38
	v_cvt_f32_ubyte1_e32 v86, v38
	v_cvt_f32_ubyte2_e32 v87, v38
	v_cvt_f32_ubyte3_e32 v88, v38
	v_fmac_f32_e32 v10, v85, v56
	v_fmac_f32_e32 v11, v86, v56
	v_fmac_f32_e32 v12, v87, v56
	v_fmac_f32_e32 v13, v88, v56
	v_cvt_f32_ubyte0_e32 v85, v39
	v_cvt_f32_ubyte1_e32 v86, v39
	v_cvt_f32_ubyte2_e32 v87, v39
	v_cvt_f32_ubyte3_e32 v88, v39
	v_fmac_f32_e32 v14, v85, v56
	v_fmac_f32_e32 v15, v86, v56
	v_fmac_f32_e32 v16, v87, v56
	v_fmac_f32_e32 v17, v88, v56
	v_add_f32_e32 v18, v18, v56
	v_and_b32_e32 v84, 0xffff, v79
	v_lshl_or_b32 v83, v84, 7, v89
	v_cmp_lt_i32_e32 vcc, 12, v78
	s_mov_b64 exec, vcc
	global_load_dwordx4 v[36:39], v83, s[12:13]
	s_mov_b64 exec, -1
	v_cvt_f32_f16_e32 v56, v81
	s_waitcnt vmcnt(7)
	v_cvt_f32_ubyte0_e32 v85, v40
	v_cvt_f32_ubyte1_e32 v86, v40
	v_cvt_f32_ubyte2_e32 v87, v40
	v_cvt_f32_ubyte3_e32 v88, v40
	v_fmac_f32_e32 v2, v85, v57
	v_fmac_f32_e32 v3, v86, v57
	v_fmac_f32_e32 v4, v87, v57
	v_fmac_f32_e32 v5, v88, v57
	v_cvt_f32_ubyte0_e32 v85, v41
	v_cvt_f32_ubyte1_e32 v86, v41
	v_cvt_f32_ubyte2_e32 v87, v41
	v_cvt_f32_ubyte3_e32 v88, v41
	v_fmac_f32_e32 v6, v85, v57
	v_fmac_f32_e32 v7, v86, v57
	v_fmac_f32_e32 v8, v87, v57
	v_fmac_f32_e32 v9, v88, v57
	v_cvt_f32_ubyte0_e32 v85, v42
	v_cvt_f32_ubyte1_e32 v86, v42
	v_cvt_f32_ubyte2_e32 v87, v42
	v_cvt_f32_ubyte3_e32 v88, v42
	v_fmac_f32_e32 v10, v85, v57
	v_fmac_f32_e32 v11, v86, v57
	v_fmac_f32_e32 v12, v87, v57
	v_fmac_f32_e32 v13, v88, v57
	v_cvt_f32_ubyte0_e32 v85, v43
	v_cvt_f32_ubyte1_e32 v86, v43
	v_cvt_f32_ubyte2_e32 v87, v43
	v_cvt_f32_ubyte3_e32 v88, v43
	v_fmac_f32_e32 v14, v85, v57
	v_fmac_f32_e32 v15, v86, v57
	v_fmac_f32_e32 v16, v87, v57
	v_fmac_f32_e32 v17, v88, v57
	v_add_f32_e32 v18, v18, v57
	v_lshrrev_b32_e32 v84, 16, v79
	v_lshl_or_b32 v83, v84, 7, v89
	v_cmp_lt_i32_e32 vcc, 13, v78
	s_mov_b64 exec, vcc
	global_load_dwordx4 v[40:43], v83, s[12:13]
	s_mov_b64 exec, -1
	v_cvt_f32_f16_sdwa v57, v81 dst_sel:DWORD dst_unused:UNUSED_PAD src0_sel:WORD_1
	s_waitcnt lgkmcnt(0)
	ds_bpermute_b32 v79, v90, v74 offset:0
	ds_bpermute_b32 v81, v90, v76 offset:0
	s_waitcnt vmcnt(7)
	v_cvt_f32_ubyte0_e32 v85, v44
	v_cvt_f32_ubyte1_e32 v86, v44
	v_cvt_f32_ubyte2_e32 v87, v44
	v_cvt_f32_ubyte3_e32 v88, v44
	v_fmac_f32_e32 v2, v85, v58
	v_fmac_f32_e32 v3, v86, v58
	v_fmac_f32_e32 v4, v87, v58
	v_fmac_f32_e32 v5, v88, v58
	v_cvt_f32_ubyte0_e32 v85, v45
	v_cvt_f32_ubyte1_e32 v86, v45
	v_cvt_f32_ubyte2_e32 v87, v45
	v_cvt_f32_ubyte3_e32 v88, v45
	v_fmac_f32_e32 v6, v85, v58
	v_fmac_f32_e32 v7, v86, v58
	v_fmac_f32_e32 v8, v87, v58
	v_fmac_f32_e32 v9, v88, v58
	v_cvt_f32_ubyte0_e32 v85, v46
	v_cvt_f32_ubyte1_e32 v86, v46
	v_cvt_f32_ubyte2_e32 v87, v46
	v_cvt_f32_ubyte3_e32 v88, v46
	v_fmac_f32_e32 v10, v85, v58
	v_fmac_f32_e32 v11, v86, v58
	v_fmac_f32_e32 v12, v87, v58
	v_fmac_f32_e32 v13, v88, v58
	v_cvt_f32_ubyte0_e32 v85, v47
	v_cvt_f32_ubyte1_e32 v86, v47
	v_cvt_f32_ubyte2_e32 v87, v47
	v_cvt_f32_ubyte3_e32 v88, v47
	v_fmac_f32_e32 v14, v85, v58
	v_fmac_f32_e32 v15, v86, v58
	v_fmac_f32_e32 v16, v87, v58
	v_fmac_f32_e32 v17, v88, v58
	v_add_f32_e32 v18, v18, v58
	v_and_b32_e32 v84, 0xffff, v80
	v_lshl_or_b32 v83, v84, 7, v89
	v_cmp_lt_i32_e32 vcc, 14, v78
	s_mov_b64 exec, vcc
	global_load_dwordx4 v[44:47], v83, s[12:13]
	s_mov_b64 exec, -1
	v_cvt_f32_f16_e32 v58, v82
	s_waitcnt vmcnt(7)
	v_cvt_f32_ubyte0_e32 v85, v48
	v_cvt_f32_ubyte1_e32 v86, v48
	v_cvt_f32_ubyte2_e32 v87, v48
	v_cvt_f32_ubyte3_e32 v88, v48
	v_fmac_f32_e32 v2, v85, v59
	v_fmac_f32_e32 v3, v86, v59
	v_fmac_f32_e32 v4, v87, v59
	v_fmac_f32_e32 v5, v88, v59
	v_cvt_f32_ubyte0_e32 v85, v49
	v_cvt_f32_ubyte1_e32 v86, v49
	v_cvt_f32_ubyte2_e32 v87, v49
	v_cvt_f32_ubyte3_e32 v88, v49
	v_fmac_f32_e32 v6, v85, v59
	v_fmac_f32_e32 v7, v86, v59
	v_fmac_f32_e32 v8, v87, v59
	v_fmac_f32_e32 v9, v88, v59
	v_cvt_f32_ubyte0_e32 v85, v50
	v_cvt_f32_ubyte1_e32 v86, v50
	v_cvt_f32_ubyte2_e32 v87, v50
	v_cvt_f32_ubyte3_e32 v88, v50
	v_fmac_f32_e32 v10, v85, v59
	v_fmac_f32_e32 v11, v86, v59
	v_fmac_f32_e32 v12, v87, v59
	v_fmac_f32_e32 v13, v88, v59
	v_cvt_f32_ubyte0_e32 v85, v51
	v_cvt_f32_ubyte1_e32 v86, v51
	v_cvt_f32_ubyte2_e32 v87, v51
	v_cvt_f32_ubyte3_e32 v88, v51
	v_fmac_f32_e32 v14, v85, v59
	v_fmac_f32_e32 v15, v86, v59
	v_fmac_f32_e32 v16, v87, v59
	v_fmac_f32_e32 v17, v88, v59
	v_add_f32_e32 v18, v18, v59
	v_lshrrev_b32_e32 v84, 16, v80
	v_lshl_or_b32 v83, v84, 7, v89
	v_cmp_lt_i32_e32 vcc, 15, v78
	s_mov_b64 exec, vcc
	global_load_dwordx4 v[48:51], v83, s[12:13]
	s_mov_b64 exec, -1
	v_cvt_f32_f16_sdwa v59, v82 dst_sel:DWORD dst_unused:UNUSED_PAD src0_sel:WORD_1
	s_cmp_le_u32 s40, 16
	s_cbranch_scc1 .Lg1_tail0
	s_waitcnt lgkmcnt(0)
	ds_bpermute_b32 v80, v90, v74 offset:4
	ds_bpermute_b32 v82, v90, v76 offset:4
	s_waitcnt vmcnt(7)
	v_cvt_f32_ubyte0_e32 v85, v20
	v_cvt_f32_ubyte1_e32 v86, v20
	v_cvt_f32_ubyte2_e32 v87, v20
	v_cvt_f32_ubyte3_e32 v88, v20
	v_fmac_f32_e32 v2, v85, v52
	v_fmac_f32_e32 v3, v86, v52
	v_fmac_f32_e32 v4, v87, v52
	v_fmac_f32_e32 v5, v88, v52
	v_cvt_f32_ubyte0_e32 v85, v21
	v_cvt_f32_ubyte1_e32 v86, v21
	v_cvt_f32_ubyte2_e32 v87, v21
	v_cvt_f32_ubyte3_e32 v88, v21
	v_fmac_f32_e32 v6, v85, v52
	v_fmac_f32_e32 v7, v86, v52
	v_fmac_f32_e32 v8, v87, v52
	v_fmac_f32_e32 v9, v88, v52
	v_cvt_f32_ubyte0_e32 v85, v22
	v_cvt_f32_ubyte1_e32 v86, v22
	v_cvt_f32_ubyte2_e32 v87, v22
	v_cvt_f32_ubyte3_e32 v88, v22
	v_fmac_f32_e32 v10, v85, v52
	v_fmac_f32_e32 v11, v86, v52
	v_fmac_f32_e32 v12, v87, v52
	v_fmac_f32_e32 v13, v88, v52
	v_cvt_f32_ubyte0_e32 v85, v23
	v_cvt_f32_ubyte1_e32 v86, v23
	v_cvt_f32_ubyte2_e32 v87, v23
	v_cvt_f32_ubyte3_e32 v88, v23
	v_fmac_f32_e32 v14, v85, v52
	v_fmac_f32_e32 v15, v86, v52
	v_fmac_f32_e32 v16, v87, v52
	v_fmac_f32_e32 v17, v88, v52
	v_add_f32_e32 v18, v18, v52
	v_and_b32_e32 v84, 0xffff, v79
	v_lshl_or_b32 v83, v84, 7, v89
	v_cmp_lt_i32_e32 vcc, 16, v78
	s_mov_b64 exec, vcc
	global_load_dwordx4 v[20:23], v83, s[12:13]
	s_mov_b64 exec, -1
	v_cvt_f32_f16_e32 v52, v81
	s_waitcnt vmcnt(7)
	v_cvt_f32_ubyte0_e32 v85, v24
	v_cvt_f32_ubyte1_e32 v86, v24
	v_cvt_f32_ubyte2_e32 v87, v24
	v_cvt_f32_ubyte3_e32 v88, v24
	v_fmac_f32_e32 v2, v85, v53
	v_fmac_f32_e32 v3, v86, v53
	v_fmac_f32_e32 v4, v87, v53
	v_fmac_f32_e32 v5, v88, v53
	v_cvt_f32_ubyte0_e32 v85, v25
	v_cvt_f32_ubyte1_e32 v86, v25
	v_cvt_f32_ubyte2_e32 v87, v25
	v_cvt_f32_ubyte3_e32 v88, v25
	v_fmac_f32_e32 v6, v85, v53
	v_fmac_f32_e32 v7, v86, v53
	v_fmac_f32_e32 v8, v87, v53
	v_fmac_f32_e32 v9, v88, v53
	v_cvt_f32_ubyte0_e32 v85, v26
	v_cvt_f32_ubyte1_e32 v86, v26
	v_cvt_f32_ubyte2_e32 v87, v26
	v_cvt_f32_ubyte3_e32 v88, v26
	v_fmac_f32_e32 v10, v85, v53
	v_fmac_f32_e32 v11, v86, v53
	v_fmac_f32_e32 v12, v87, v53
	v_fmac_f32_e32 v13, v88, v53
	v_cvt_f32_ubyte0_e32 v85, v27
	v_cvt_f32_ubyte1_e32 v86, v27
	v_cvt_f32_ubyte2_e32 v87, v27
	v_cvt_f32_ubyte3_e32 v88, v27
	v_fmac_f32_e32 v14, v85, v53
	v_fmac_f32_e32 v15, v86, v53
	v_fmac_f32_e32 v16, v87, v53
	v_fmac_f32_e32 v17, v88, v53
	v_add_f32_e32 v18, v18, v53
	v_lshrrev_b32_e32 v84, 16, v79
	v_lshl_or_b32 v83, v84, 7, v89
	v_cmp_lt_i32_e32 vcc, 17, v78
	s_mov_b64 exec, vcc
	global_load_dwordx4 v[24:27], v83, s[12:13]
	s_mov_b64 exec, -1
	v_cvt_f32_f16_sdwa v53, v81 dst_sel:DWORD dst_unused:UNUSED_PAD src0_sel:WORD_1
	s_waitcnt lgkmcnt(0)
	ds_bpermute_b32 v79, v90, v74 offset:8
	ds_bpermute_b32 v81, v90, v76 offset:8
	s_waitcnt vmcnt(7)
	v_cvt_f32_ubyte0_e32 v85, v28
	v_cvt_f32_ubyte1_e32 v86, v28
	v_cvt_f32_ubyte2_e32 v87, v28
	v_cvt_f32_ubyte3_e32 v88, v28
	v_fmac_f32_e32 v2, v85, v54
	v_fmac_f32_e32 v3, v86, v54
	v_fmac_f32_e32 v4, v87, v54
	v_fmac_f32_e32 v5, v88, v54
	v_cvt_f32_ubyte0_e32 v85, v29
	v_cvt_f32_ubyte1_e32 v86, v29
	v_cvt_f32_ubyte2_e32 v87, v29
	v_cvt_f32_ubyte3_e32 v88, v29
	v_fmac_f32_e32 v6, v85, v54
	v_fmac_f32_e32 v7, v86, v54
	v_fmac_f32_e32 v8, v87, v54
	v_fmac_f32_e32 v9, v88, v54
	v_cvt_f32_ubyte0_e32 v85, v30
	v_cvt_f32_ubyte1_e32 v86, v30
	v_cvt_f32_ubyte2_e32 v87, v30
	v_cvt_f32_ubyte3_e32 v88, v30
	v_fmac_f32_e32 v10, v85, v54
	v_fmac_f32_e32 v11, v86, v54
	v_fmac_f32_e32 v12, v87, v54
	v_fmac_f32_e32 v13, v88, v54
	v_cvt_f32_ubyte0_e32 v85, v31
	v_cvt_f32_ubyte1_e32 v86, v31
	v_cvt_f32_ubyte2_e32 v87, v31
	v_cvt_f32_ubyte3_e32 v88, v31
	v_fmac_f32_e32 v14, v85, v54
	v_fmac_f32_e32 v15, v86, v54
	v_fmac_f32_e32 v16, v87, v54
	v_fmac_f32_e32 v17, v88, v54
	v_add_f32_e32 v18, v18, v54
	v_and_b32_e32 v84, 0xffff, v80
	v_lshl_or_b32 v83, v84, 7, v89
	v_cmp_lt_i32_e32 vcc, 18, v78
	s_mov_b64 exec, vcc
	global_load_dwordx4 v[28:31], v83, s[12:13]
	s_mov_b64 exec, -1
	v_cvt_f32_f16_e32 v54, v82
	s_waitcnt vmcnt(7)
	v_cvt_f32_ubyte0_e32 v85, v32
	v_cvt_f32_ubyte1_e32 v86, v32
	v_cvt_f32_ubyte2_e32 v87, v32
	v_cvt_f32_ubyte3_e32 v88, v32
	v_fmac_f32_e32 v2, v85, v55
	v_fmac_f32_e32 v3, v86, v55
	v_fmac_f32_e32 v4, v87, v55
	v_fmac_f32_e32 v5, v88, v55
	v_cvt_f32_ubyte0_e32 v85, v33
	v_cvt_f32_ubyte1_e32 v86, v33
	v_cvt_f32_ubyte2_e32 v87, v33
	v_cvt_f32_ubyte3_e32 v88, v33
	v_fmac_f32_e32 v6, v85, v55
	v_fmac_f32_e32 v7, v86, v55
	v_fmac_f32_e32 v8, v87, v55
	v_fmac_f32_e32 v9, v88, v55
	v_cvt_f32_ubyte0_e32 v85, v34
	v_cvt_f32_ubyte1_e32 v86, v34
	v_cvt_f32_ubyte2_e32 v87, v34
	v_cvt_f32_ubyte3_e32 v88, v34
	v_fmac_f32_e32 v10, v85, v55
	v_fmac_f32_e32 v11, v86, v55
	v_fmac_f32_e32 v12, v87, v55
	v_fmac_f32_e32 v13, v88, v55
	v_cvt_f32_ubyte0_e32 v85, v35
	v_cvt_f32_ubyte1_e32 v86, v35
	v_cvt_f32_ubyte2_e32 v87, v35
	v_cvt_f32_ubyte3_e32 v88, v35
	v_fmac_f32_e32 v14, v85, v55
	v_fmac_f32_e32 v15, v86, v55
	v_fmac_f32_e32 v16, v87, v55
	v_fmac_f32_e32 v17, v88, v55
	v_add_f32_e32 v18, v18, v55
	v_lshrrev_b32_e32 v84, 16, v80
	v_lshl_or_b32 v83, v84, 7, v89
	v_cmp_lt_i32_e32 vcc, 19, v78
	s_mov_b64 exec, vcc
	global_load_dwordx4 v[32:35], v83, s[12:13]
	s_mov_b64 exec, -1
	v_cvt_f32_f16_sdwa v55, v82 dst_sel:DWORD dst_unused:UNUSED_PAD src0_sel:WORD_1
	s_cmp_le_u32 s40, 20
	s_cbranch_scc1 .Lg1_tail4
	s_waitcnt lgkmcnt(0)
	ds_bpermute_b32 v80, v90, v74 offset:12
	ds_bpermute_b32 v82, v90, v76 offset:12
	s_waitcnt vmcnt(7)
	v_cvt_f32_ubyte0_e32 v85, v36
	v_cvt_f32_ubyte1_e32 v86, v36
	v_cvt_f32_ubyte2_e32 v87, v36
	v_cvt_f32_ubyte3_e32 v88, v36
	v_fmac_f32_e32 v2, v85, v56
	v_fmac_f32_e32 v3, v86, v56
	v_fmac_f32_e32 v4, v87, v56
	v_fmac_f32_e32 v5, v88, v56
	v_cvt_f32_ubyte0_e32 v85, v37
	v_cvt_f32_ubyte1_e32 v86, v37
	v_cvt_f32_ubyte2_e32 v87, v37
	v_cvt_f32_ubyte3_e32 v88, v37
	v_fmac_f32_e32 v6, v85, v56
	v_fmac_f32_e32 v7, v86, v56
	v_fmac_f32_e32 v8, v87, v56
	v_fmac_f32_e32 v9, v88, v56
	v_cvt_f32_ubyte0_e32 v85, v38
	v_cvt_f32_ubyte1_e32 v86, v38
	v_cvt_f32_ubyte2_e32 v87, v38
	v_cvt_f32_ubyte3_e32 v88, v38
	v_fmac_f32_e32 v10, v85, v56
	v_fmac_f32_e32 v11, v86, v56
	v_fmac_f32_e32 v12, v87, v56
	v_fmac_f32_e32 v13, v88, v56
	v_cvt_f32_ubyte0_e32 v85, v39
	v_cvt_f32_ubyte1_e32 v86, v39
	v_cvt_f32_ubyte2_e32 v87, v39
	v_cvt_f32_ubyte3_e32 v88, v39
	v_fmac_f32_e32 v14, v85, v56
	v_fmac_f32_e32 v15, v86, v56
	v_fmac_f32_e32 v16, v87, v56
	v_fmac_f32_e32 v17, v88, v56
	v_add_f32_e32 v18, v18, v56
	v_and_b32_e32 v84, 0xffff, v79
	v_lshl_or_b32 v83, v84, 7, v89
	v_cmp_lt_i32_e32 vcc, 20, v78
	s_mov_b64 exec, vcc
	global_load_dwordx4 v[36:39], v83, s[12:13]
	s_mov_b64 exec, -1
	v_cvt_f32_f16_e32 v56, v81
	s_waitcnt vmcnt(7)
	v_cvt_f32_ubyte0_e32 v85, v40
	v_cvt_f32_ubyte1_e32 v86, v40
	v_cvt_f32_ubyte2_e32 v87, v40
	v_cvt_f32_ubyte3_e32 v88, v40
	v_fmac_f32_e32 v2, v85, v57
	v_fmac_f32_e32 v3, v86, v57
	v_fmac_f32_e32 v4, v87, v57
	v_fmac_f32_e32 v5, v88, v57
	v_cvt_f32_ubyte0_e32 v85, v41
	v_cvt_f32_ubyte1_e32 v86, v41
	v_cvt_f32_ubyte2_e32 v87, v41
	v_cvt_f32_ubyte3_e32 v88, v41
	v_fmac_f32_e32 v6, v85, v57
	v_fmac_f32_e32 v7, v86, v57
	v_fmac_f32_e32 v8, v87, v57
	v_fmac_f32_e32 v9, v88, v57
	v_cvt_f32_ubyte0_e32 v85, v42
	v_cvt_f32_ubyte1_e32 v86, v42
	v_cvt_f32_ubyte2_e32 v87, v42
	v_cvt_f32_ubyte3_e32 v88, v42
	v_fmac_f32_e32 v10, v85, v57
	v_fmac_f32_e32 v11, v86, v57
	v_fmac_f32_e32 v12, v87, v57
	v_fmac_f32_e32 v13, v88, v57
	v_cvt_f32_ubyte0_e32 v85, v43
	v_cvt_f32_ubyte1_e32 v86, v43
	v_cvt_f32_ubyte2_e32 v87, v43
	v_cvt_f32_ubyte3_e32 v88, v43
	v_fmac_f32_e32 v14, v85, v57
	v_fmac_f32_e32 v15, v86, v57
	v_fmac_f32_e32 v16, v87, v57
	v_fmac_f32_e32 v17, v88, v57
	v_add_f32_e32 v18, v18, v57
	v_lshrrev_b32_e32 v84, 16, v79
	v_lshl_or_b32 v83, v84, 7, v89
	v_cmp_lt_i32_e32 vcc, 21, v78
	s_mov_b64 exec, vcc
	global_load_dwordx4 v[40:43], v83, s[12:13]
	s_mov_b64 exec, -1
	v_cvt_f32_f16_sdwa v57, v81 dst_sel:DWORD dst_unused:UNUSED_PAD src0_sel:WORD_1
	s_waitcnt lgkmcnt(0)
	ds_bpermute_b32 v79, v90, v74 offset:16
	ds_bpermute_b32 v81, v90, v76 offset:16
	s_waitcnt vmcnt(7)
	v_cvt_f32_ubyte0_e32 v85, v44
	v_cvt_f32_ubyte1_e32 v86, v44
	v_cvt_f32_ubyte2_e32 v87, v44
	v_cvt_f32_ubyte3_e32 v88, v44
	v_fmac_f32_e32 v2, v85, v58
	v_fmac_f32_e32 v3, v86, v58
	v_fmac_f32_e32 v4, v87, v58
	v_fmac_f32_e32 v5, v88, v58
	v_cvt_f32_ubyte0_e32 v85, v45
	v_cvt_f32_ubyte1_e32 v86, v45
	v_cvt_f32_ubyte2_e32 v87, v45
	v_cvt_f32_ubyte3_e32 v88, v45
	v_fmac_f32_e32 v6, v85, v58
	v_fmac_f32_e32 v7, v86, v58
	v_fmac_f32_e32 v8, v87, v58
	v_fmac_f32_e32 v9, v88, v58
	v_cvt_f32_ubyte0_e32 v85, v46
	v_cvt_f32_ubyte1_e32 v86, v46
	v_cvt_f32_ubyte2_e32 v87, v46
	v_cvt_f32_ubyte3_e32 v88, v46
	v_fmac_f32_e32 v10, v85, v58
	v_fmac_f32_e32 v11, v86, v58
	v_fmac_f32_e32 v12, v87, v58
	v_fmac_f32_e32 v13, v88, v58
	v_cvt_f32_ubyte0_e32 v85, v47
	v_cvt_f32_ubyte1_e32 v86, v47
	v_cvt_f32_ubyte2_e32 v87, v47
	v_cvt_f32_ubyte3_e32 v88, v47
	v_fmac_f32_e32 v14, v85, v58
	v_fmac_f32_e32 v15, v86, v58
	v_fmac_f32_e32 v16, v87, v58
	v_fmac_f32_e32 v17, v88, v58
	v_add_f32_e32 v18, v18, v58
	v_and_b32_e32 v84, 0xffff, v80
	v_lshl_or_b32 v83, v84, 7, v89
	v_cmp_lt_i32_e32 vcc, 22, v78
	s_mov_b64 exec, vcc
	global_load_dwordx4 v[44:47], v83, s[12:13]
	s_mov_b64 exec, -1
	v_cvt_f32_f16_e32 v58, v82
	s_waitcnt vmcnt(7)
	v_cvt_f32_ubyte0_e32 v85, v48
	v_cvt_f32_ubyte1_e32 v86, v48
	v_cvt_f32_ubyte2_e32 v87, v48
	v_cvt_f32_ubyte3_e32 v88, v48
	v_fmac_f32_e32 v2, v85, v59
	v_fmac_f32_e32 v3, v86, v59
	v_fmac_f32_e32 v4, v87, v59
	v_fmac_f32_e32 v5, v88, v59
	v_cvt_f32_ubyte0_e32 v85, v49
	v_cvt_f32_ubyte1_e32 v86, v49
	v_cvt_f32_ubyte2_e32 v87, v49
	v_cvt_f32_ubyte3_e32 v88, v49
	v_fmac_f32_e32 v6, v85, v59
	v_fmac_f32_e32 v7, v86, v59
	v_fmac_f32_e32 v8, v87, v59
	v_fmac_f32_e32 v9, v88, v59
	v_cvt_f32_ubyte0_e32 v85, v50
	v_cvt_f32_ubyte1_e32 v86, v50
	v_cvt_f32_ubyte2_e32 v87, v50
	v_cvt_f32_ubyte3_e32 v88, v50
	v_fmac_f32_e32 v10, v85, v59
	v_fmac_f32_e32 v11, v86, v59
	v_fmac_f32_e32 v12, v87, v59
	v_fmac_f32_e32 v13, v88, v59
	v_cvt_f32_ubyte0_e32 v85, v51
	v_cvt_f32_ubyte1_e32 v86, v51
	v_cvt_f32_ubyte2_e32 v87, v51
	v_cvt_f32_ubyte3_e32 v88, v51
	v_fmac_f32_e32 v14, v85, v59
	v_fmac_f32_e32 v15, v86, v59
	v_fmac_f32_e32 v16, v87, v59
	v_fmac_f32_e32 v17, v88, v59
	v_add_f32_e32 v18, v18, v59
	v_lshrrev_b32_e32 v84, 16, v80
	v_lshl_or_b32 v83, v84, 7, v89
	v_cmp_lt_i32_e32 vcc, 23, v78
	s_mov_b64 exec, vcc
	global_load_dwordx4 v[48:51], v83, s[12:13]
	s_mov_b64 exec, -1
	v_cvt_f32_f16_sdwa v59, v82 dst_sel:DWORD dst_unused:UNUSED_PAD src0_sel:WORD_1
	s_cmp_le_u32 s40, 24
	s_cbranch_scc1 .Lg1_tail0
	s_waitcnt lgkmcnt(0)
	ds_bpermute_b32 v80, v90, v74 offset:20
	ds_bpermute_b32 v82, v90, v76 offset:20
	s_waitcnt vmcnt(7)
	v_cvt_f32_ubyte0_e32 v85, v20
	v_cvt_f32_ubyte1_e32 v86, v20
	v_cvt_f32_ubyte2_e32 v87, v20
	v_cvt_f32_ubyte3_e32 v88, v20
	v_fmac_f32_e32 v2, v85, v52
	v_fmac_f32_e32 v3, v86, v52
	v_fmac_f32_e32 v4, v87, v52
	v_fmac_f32_e32 v5, v88, v52
	v_cvt_f32_ubyte0_e32 v85, v21
	v_cvt_f32_ubyte1_e32 v86, v21
	v_cvt_f32_ubyte2_e32 v87, v21
	v_cvt_f32_ubyte3_e32 v88, v21
	v_fmac_f32_e32 v6, v85, v52
	v_fmac_f32_e32 v7, v86, v52
	v_fmac_f32_e32 v8, v87, v52
	v_fmac_f32_e32 v9, v88, v52
	v_cvt_f32_ubyte0_e32 v85, v22
	v_cvt_f32_ubyte1_e32 v86, v22
	v_cvt_f32_ubyte2_e32 v87, v22
	v_cvt_f32_ubyte3_e32 v88, v22
	v_fmac_f32_e32 v10, v85, v52
	v_fmac_f32_e32 v11, v86, v52
	v_fmac_f32_e32 v12, v87, v52
	v_fmac_f32_e32 v13, v88, v52
	v_cvt_f32_ubyte0_e32 v85, v23
	v_cvt_f32_ubyte1_e32 v86, v23
	v_cvt_f32_ubyte2_e32 v87, v23
	v_cvt_f32_ubyte3_e32 v88, v23
	v_fmac_f32_e32 v14, v85, v52
	v_fmac_f32_e32 v15, v86, v52
	v_fmac_f32_e32 v16, v87, v52
	v_fmac_f32_e32 v17, v88, v52
	v_add_f32_e32 v18, v18, v52
	v_and_b32_e32 v84, 0xffff, v79
	v_lshl_or_b32 v83, v84, 7, v89
	v_cmp_lt_i32_e32 vcc, 24, v78
	s_mov_b64 exec, vcc
	global_load_dwordx4 v[20:23], v83, s[12:13]
	s_mov_b64 exec, -1
	v_cvt_f32_f16_e32 v52, v81
	s_waitcnt vmcnt(7)
	v_cvt_f32_ubyte0_e32 v85, v24
	v_cvt_f32_ubyte1_e32 v86, v24
	v_cvt_f32_ubyte2_e32 v87, v24
	v_cvt_f32_ubyte3_e32 v88, v24
	v_fmac_f32_e32 v2, v85, v53
	v_fmac_f32_e32 v3, v86, v53
	v_fmac_f32_e32 v4, v87, v53
	v_fmac_f32_e32 v5, v88, v53
	v_cvt_f32_ubyte0_e32 v85, v25
	v_cvt_f32_ubyte1_e32 v86, v25
	v_cvt_f32_ubyte2_e32 v87, v25
	v_cvt_f32_ubyte3_e32 v88, v25
	v_fmac_f32_e32 v6, v85, v53
	v_fmac_f32_e32 v7, v86, v53
	v_fmac_f32_e32 v8, v87, v53
	v_fmac_f32_e32 v9, v88, v53
	v_cvt_f32_ubyte0_e32 v85, v26
	v_cvt_f32_ubyte1_e32 v86, v26
	v_cvt_f32_ubyte2_e32 v87, v26
	v_cvt_f32_ubyte3_e32 v88, v26
	v_fmac_f32_e32 v10, v85, v53
	v_fmac_f32_e32 v11, v86, v53
	v_fmac_f32_e32 v12, v87, v53
	v_fmac_f32_e32 v13, v88, v53
	v_cvt_f32_ubyte0_e32 v85, v27
	v_cvt_f32_ubyte1_e32 v86, v27
	v_cvt_f32_ubyte2_e32 v87, v27
	v_cvt_f32_ubyte3_e32 v88, v27
	v_fmac_f32_e32 v14, v85, v53
	v_fmac_f32_e32 v15, v86, v53
	v_fmac_f32_e32 v16, v87, v53
	v_fmac_f32_e32 v17, v88, v53
	v_add_f32_e32 v18, v18, v53
	v_lshrrev_b32_e32 v84, 16, v79
	v_lshl_or_b32 v83, v84, 7, v89
	v_cmp_lt_i32_e32 vcc, 25, v78
	s_mov_b64 exec, vcc
	global_load_dwordx4 v[24:27], v83, s[12:13]
	s_mov_b64 exec, -1
	v_cvt_f32_f16_sdwa v53, v81 dst_sel:DWORD dst_unused:UNUSED_PAD src0_sel:WORD_1
	s_waitcnt lgkmcnt(0)
	ds_bpermute_b32 v79, v90, v74 offset:24
	ds_bpermute_b32 v81, v90, v76 offset:24
	s_waitcnt vmcnt(7)
	v_cvt_f32_ubyte0_e32 v85, v28
	v_cvt_f32_ubyte1_e32 v86, v28
	v_cvt_f32_ubyte2_e32 v87, v28
	v_cvt_f32_ubyte3_e32 v88, v28
	v_fmac_f32_e32 v2, v85, v54
	v_fmac_f32_e32 v3, v86, v54
	v_fmac_f32_e32 v4, v87, v54
	v_fmac_f32_e32 v5, v88, v54
	v_cvt_f32_ubyte0_e32 v85, v29
	v_cvt_f32_ubyte1_e32 v86, v29
	v_cvt_f32_ubyte2_e32 v87, v29
	v_cvt_f32_ubyte3_e32 v88, v29
	v_fmac_f32_e32 v6, v85, v54
	v_fmac_f32_e32 v7, v86, v54
	v_fmac_f32_e32 v8, v87, v54
	v_fmac_f32_e32 v9, v88, v54
	v_cvt_f32_ubyte0_e32 v85, v30
	v_cvt_f32_ubyte1_e32 v86, v30
	v_cvt_f32_ubyte2_e32 v87, v30
	v_cvt_f32_ubyte3_e32 v88, v30
	v_fmac_f32_e32 v10, v85, v54
	v_fmac_f32_e32 v11, v86, v54
	v_fmac_f32_e32 v12, v87, v54
	v_fmac_f32_e32 v13, v88, v54
	v_cvt_f32_ubyte0_e32 v85, v31
	v_cvt_f32_ubyte1_e32 v86, v31
	v_cvt_f32_ubyte2_e32 v87, v31
	v_cvt_f32_ubyte3_e32 v88, v31
	v_fmac_f32_e32 v14, v85, v54
	v_fmac_f32_e32 v15, v86, v54
	v_fmac_f32_e32 v16, v87, v54
	v_fmac_f32_e32 v17, v88, v54
	v_add_f32_e32 v18, v18, v54
	v_and_b32_e32 v84, 0xffff, v80
	v_lshl_or_b32 v83, v84, 7, v89
	v_cmp_lt_i32_e32 vcc, 26, v78
	s_mov_b64 exec, vcc
	global_load_dwordx4 v[28:31], v83, s[12:13]
	s_mov_b64 exec, -1
	v_cvt_f32_f16_e32 v54, v82
	s_waitcnt vmcnt(7)
	v_cvt_f32_ubyte0_e32 v85, v32
	v_cvt_f32_ubyte1_e32 v86, v32
	v_cvt_f32_ubyte2_e32 v87, v32
	v_cvt_f32_ubyte3_e32 v88, v32
	v_fmac_f32_e32 v2, v85, v55
	v_fmac_f32_e32 v3, v86, v55
	v_fmac_f32_e32 v4, v87, v55
	v_fmac_f32_e32 v5, v88, v55
	v_cvt_f32_ubyte0_e32 v85, v33
	v_cvt_f32_ubyte1_e32 v86, v33
	v_cvt_f32_ubyte2_e32 v87, v33
	v_cvt_f32_ubyte3_e32 v88, v33
	v_fmac_f32_e32 v6, v85, v55
	v_fmac_f32_e32 v7, v86, v55
	v_fmac_f32_e32 v8, v87, v55
	v_fmac_f32_e32 v9, v88, v55
	v_cvt_f32_ubyte0_e32 v85, v34
	v_cvt_f32_ubyte1_e32 v86, v34
	v_cvt_f32_ubyte2_e32 v87, v34
	v_cvt_f32_ubyte3_e32 v88, v34
	v_fmac_f32_e32 v10, v85, v55
	v_fmac_f32_e32 v11, v86, v55
	v_fmac_f32_e32 v12, v87, v55
	v_fmac_f32_e32 v13, v88, v55
	v_cvt_f32_ubyte0_e32 v85, v35
	v_cvt_f32_ubyte1_e32 v86, v35
	v_cvt_f32_ubyte2_e32 v87, v35
	v_cvt_f32_ubyte3_e32 v88, v35
	v_fmac_f32_e32 v14, v85, v55
	v_fmac_f32_e32 v15, v86, v55
	v_fmac_f32_e32 v16, v87, v55
	v_fmac_f32_e32 v17, v88, v55
	v_add_f32_e32 v18, v18, v55
	v_lshrrev_b32_e32 v84, 16, v80
	v_lshl_or_b32 v83, v84, 7, v89
	v_cmp_lt_i32_e32 vcc, 27, v78
	s_mov_b64 exec, vcc
	global_load_dwordx4 v[32:35], v83, s[12:13]
	s_mov_b64 exec, -1
	v_cvt_f32_f16_sdwa v55, v82 dst_sel:DWORD dst_unused:UNUSED_PAD src0_sel:WORD_1
	s_cmp_le_u32 s40, 28
	s_cbranch_scc1 .Lg1_tail4
	s_waitcnt lgkmcnt(0)
	ds_bpermute_b32 v80, v90, v74 offset:28
	ds_bpermute_b32 v82, v90, v76 offset:28
	s_waitcnt vmcnt(7)
	v_cvt_f32_ubyte0_e32 v85, v36
	v_cvt_f32_ubyte1_e32 v86, v36
	v_cvt_f32_ubyte2_e32 v87, v36
	v_cvt_f32_ubyte3_e32 v88, v36
	v_fmac_f32_e32 v2, v85, v56
	v_fmac_f32_e32 v3, v86, v56
	v_fmac_f32_e32 v4, v87, v56
	v_fmac_f32_e32 v5, v88, v56
	v_cvt_f32_ubyte0_e32 v85, v37
	v_cvt_f32_ubyte1_e32 v86, v37
	v_cvt_f32_ubyte2_e32 v87, v37
	v_cvt_f32_ubyte3_e32 v88, v37
	v_fmac_f32_e32 v6, v85, v56
	v_fmac_f32_e32 v7, v86, v56
	v_fmac_f32_e32 v8, v87, v56
	v_fmac_f32_e32 v9, v88, v56
	v_cvt_f32_ubyte0_e32 v85, v38
	v_cvt_f32_ubyte1_e32 v86, v38
	v_cvt_f32_ubyte2_e32 v87, v38
	v_cvt_f32_ubyte3_e32 v88, v38
	v_fmac_f32_e32 v10, v85, v56
	v_fmac_f32_e32 v11, v86, v56
	v_fmac_f32_e32 v12, v87, v56
	v_fmac_f32_e32 v13, v88, v56
	v_cvt_f32_ubyte0_e32 v85, v39
	v_cvt_f32_ubyte1_e32 v86, v39
	v_cvt_f32_ubyte2_e32 v87, v39
	v_cvt_f32_ubyte3_e32 v88, v39
	v_fmac_f32_e32 v14, v85, v56
	v_fmac_f32_e32 v15, v86, v56
	v_fmac_f32_e32 v16, v87, v56
	v_fmac_f32_e32 v17, v88, v56
	v_add_f32_e32 v18, v18, v56
	v_and_b32_e32 v84, 0xffff, v79
	v_lshl_or_b32 v83, v84, 7, v89
	v_cmp_lt_i32_e32 vcc, 28, v78
	s_mov_b64 exec, vcc
	global_load_dwordx4 v[36:39], v83, s[12:13]
	s_mov_b64 exec, -1
	v_cvt_f32_f16_e32 v56, v81
	s_waitcnt vmcnt(7)
	v_cvt_f32_ubyte0_e32 v85, v40
	v_cvt_f32_ubyte1_e32 v86, v40
	v_cvt_f32_ubyte2_e32 v87, v40
	v_cvt_f32_ubyte3_e32 v88, v40
	v_fmac_f32_e32 v2, v85, v57
	v_fmac_f32_e32 v3, v86, v57
	v_fmac_f32_e32 v4, v87, v57
	v_fmac_f32_e32 v5, v88, v57
	v_cvt_f32_ubyte0_e32 v85, v41
	v_cvt_f32_ubyte1_e32 v86, v41
	v_cvt_f32_ubyte2_e32 v87, v41
	v_cvt_f32_ubyte3_e32 v88, v41
	v_fmac_f32_e32 v6, v85, v57
	v_fmac_f32_e32 v7, v86, v57
	v_fmac_f32_e32 v8, v87, v57
	v_fmac_f32_e32 v9, v88, v57
	v_cvt_f32_ubyte0_e32 v85, v42
	v_cvt_f32_ubyte1_e32 v86, v42
	v_cvt_f32_ubyte2_e32 v87, v42
	v_cvt_f32_ubyte3_e32 v88, v42
	v_fmac_f32_e32 v10, v85, v57
	v_fmac_f32_e32 v11, v86, v57
	v_fmac_f32_e32 v12, v87, v57
	v_fmac_f32_e32 v13, v88, v57
	v_cvt_f32_ubyte0_e32 v85, v43
	v_cvt_f32_ubyte1_e32 v86, v43
	v_cvt_f32_ubyte2_e32 v87, v43
	v_cvt_f32_ubyte3_e32 v88, v43
	v_fmac_f32_e32 v14, v85, v57
	v_fmac_f32_e32 v15, v86, v57
	v_fmac_f32_e32 v16, v87, v57
	v_fmac_f32_e32 v17, v88, v57
	v_add_f32_e32 v18, v18, v57
	v_lshrrev_b32_e32 v84, 16, v79
	v_lshl_or_b32 v83, v84, 7, v89
	v_cmp_lt_i32_e32 vcc, 29, v78
	s_mov_b64 exec, vcc
	global_load_dwordx4 v[40:43], v83, s[12:13]
	s_mov_b64 exec, -1
	v_cvt_f32_f16_sdwa v57, v81 dst_sel:DWORD dst_unused:UNUSED_PAD src0_sel:WORD_1
	s_waitcnt lgkmcnt(0)
	s_waitcnt vmcnt(7)
	v_cvt_f32_ubyte0_e32 v85, v44
	v_cvt_f32_ubyte1_e32 v86, v44
	v_cvt_f32_ubyte2_e32 v87, v44
	v_cvt_f32_ubyte3_e32 v88, v44
	v_fmac_f32_e32 v2, v85, v58
	v_fmac_f32_e32 v3, v86, v58
	v_fmac_f32_e32 v4, v87, v58
	v_fmac_f32_e32 v5, v88, v58
	v_cvt_f32_ubyte0_e32 v85, v45
	v_cvt_f32_ubyte1_e32 v86, v45
	v_cvt_f32_ubyte2_e32 v87, v45
	v_cvt_f32_ubyte3_e32 v88, v45
	v_fmac_f32_e32 v6, v85, v58
	v_fmac_f32_e32 v7, v86, v58
	v_fmac_f32_e32 v8, v87, v58
	v_fmac_f32_e32 v9, v88, v58
	v_cvt_f32_ubyte0_e32 v85, v46
	v_cvt_f32_ubyte1_e32 v86, v46
	v_cvt_f32_ubyte2_e32 v87, v46
	v_cvt_f32_ubyte3_e32 v88, v46
	v_fmac_f32_e32 v10, v85, v58
	v_fmac_f32_e32 v11, v86, v58
	v_fmac_f32_e32 v12, v87, v58
	v_fmac_f32_e32 v13, v88, v58
	v_cvt_f32_ubyte0_e32 v85, v47
	v_cvt_f32_ubyte1_e32 v86, v47
	v_cvt_f32_ubyte2_e32 v87, v47
	v_cvt_f32_ubyte3_e32 v88, v47
	v_fmac_f32_e32 v14, v85, v58
	v_fmac_f32_e32 v15, v86, v58
	v_fmac_f32_e32 v16, v87, v58
	v_fmac_f32_e32 v17, v88, v58
	v_add_f32_e32 v18, v18, v58
	v_and_b32_e32 v84, 0xffff, v80
	v_lshl_or_b32 v83, v84, 7, v89
	v_cmp_lt_i32_e32 vcc, 30, v78
	s_mov_b64 exec, vcc
	global_load_dwordx4 v[44:47], v83, s[12:13]
	s_mov_b64 exec, -1
	v_cvt_f32_f16_e32 v58, v82
	s_waitcnt vmcnt(7)
	v_cvt_f32_ubyte0_e32 v85, v48
	v_cvt_f32_ubyte1_e32 v86, v48
	v_cvt_f32_ubyte2_e32 v87, v48
	v_cvt_f32_ubyte3_e32 v88, v48
	v_fmac_f32_e32 v2, v85, v59
	v_fmac_f32_e32 v3, v86, v59
	v_fmac_f32_e32 v4, v87, v59
	v_fmac_f32_e32 v5, v88, v59
	v_cvt_f32_ubyte0_e32 v85, v49
	v_cvt_f32_ubyte1_e32 v86, v49
	v_cvt_f32_ubyte2_e32 v87, v49
	v_cvt_f32_ubyte3_e32 v88, v49
	v_fmac_f32_e32 v6, v85, v59
	v_fmac_f32_e32 v7, v86, v59
	v_fmac_f32_e32 v8, v87, v59
	v_fmac_f32_e32 v9, v88, v59
	v_cvt_f32_ubyte0_e32 v85, v50
	v_cvt_f32_ubyte1_e32 v86, v50
	v_cvt_f32_ubyte2_e32 v87, v50
	v_cvt_f32_ubyte3_e32 v88, v50
	v_fmac_f32_e32 v10, v85, v59
	v_fmac_f32_e32 v11, v86, v59
	v_fmac_f32_e32 v12, v87, v59
	v_fmac_f32_e32 v13, v88, v59
	v_cvt_f32_ubyte0_e32 v85, v51
	v_cvt_f32_ubyte1_e32 v86, v51
	v_cvt_f32_ubyte2_e32 v87, v51
	v_cvt_f32_ubyte3_e32 v88, v51
	v_fmac_f32_e32 v14, v85, v59
	v_fmac_f32_e32 v15, v86, v59
	v_fmac_f32_e32 v16, v87, v59
	v_fmac_f32_e32 v17, v88, v59
	v_add_f32_e32 v18, v18, v59
	v_lshrrev_b32_e32 v84, 16, v80
	v_lshl_or_b32 v83, v84, 7, v89
	v_cmp_lt_i32_e32 vcc, 31, v78
	s_mov_b64 exec, vcc
	global_load_dwordx4 v[48:51], v83, s[12:13]
	s_mov_b64 exec, -1
	v_cvt_f32_f16_sdwa v59, v82 dst_sel:DWORD dst_unused:UNUSED_PAD src0_sel:WORD_1
.Lg1_tail0:
	s_cmp_eq_u32 s39, 1
	s_cbranch_scc1 .Lg1_tailb0
	s_waitcnt vmcnt(7)
	v_cvt_f32_ubyte0_e32 v85, v20
	v_cvt_f32_ubyte1_e32 v86, v20
	v_cvt_f32_ubyte2_e32 v87, v20
	v_cvt_f32_ubyte3_e32 v88, v20
	v_fmac_f32_e32 v2, v85, v52
	v_fmac_f32_e32 v3, v86, v52
	v_fmac_f32_e32 v4, v87, v52
	v_fmac_f32_e32 v5, v88, v52
	v_cvt_f32_ubyte0_e32 v85, v21
	v_cvt_f32_ubyte1_e32 v86, v21
	v_cvt_f32_ubyte2_e32 v87, v21
	v_cvt_f32_ubyte3_e32 v88, v21
	v_fmac_f32_e32 v6, v85, v52
	v_fmac_f32_e32 v7, v86, v52
	v_fmac_f32_e32 v8, v87, v52
	v_fmac_f32_e32 v9, v88, v52
	v_cvt_f32_ubyte0_e32 v85, v22
	v_cvt_f32_ubyte1_e32 v86, v22
	v_cvt_f32_ubyte2_e32 v87, v22
	v_cvt_f32_ubyte3_e32 v88, v22
	v_fmac_f32_e32 v10, v85, v52
	v_fmac_f32_e32 v11, v86, v52
	v_fmac_f32_e32 v12, v87, v52
	v_fmac_f32_e32 v13, v88, v52
	v_cvt_f32_ubyte0_e32 v85, v23
	v_cvt_f32_ubyte1_e32 v86, v23
	v_cvt_f32_ubyte2_e32 v87, v23
	v_cvt_f32_ubyte3_e32 v88, v23
	v_fmac_f32_e32 v14, v85, v52
	v_fmac_f32_e32 v15, v86, v52
	v_fmac_f32_e32 v16, v87, v52
	v_fmac_f32_e32 v17, v88, v52
	v_add_f32_e32 v18, v18, v52
	s_waitcnt vmcnt(6)
	v_cvt_f32_ubyte0_e32 v85, v24
	v_cvt_f32_ubyte1_e32 v86, v24
	v_cvt_f32_ubyte2_e32 v87, v24
	v_cvt_f32_ubyte3_e32 v88, v24
	v_fmac_f32_e32 v2, v85, v53
	v_fmac_f32_e32 v3, v86, v53
	v_fmac_f32_e32 v4, v87, v53
	v_fmac_f32_e32 v5, v88, v53
	v_cvt_f32_ubyte0_e32 v85, v25
	v_cvt_f32_ubyte1_e32 v86, v25
	v_cvt_f32_ubyte2_e32 v87, v25
	v_cvt_f32_ubyte3_e32 v88, v25
	v_fmac_f32_e32 v6, v85, v53
	v_fmac_f32_e32 v7, v86, v53
	v_fmac_f32_e32 v8, v87, v53
	v_fmac_f32_e32 v9, v88, v53
	v_cvt_f32_ubyte0_e32 v85, v26
	v_cvt_f32_ubyte1_e32 v86, v26
	v_cvt_f32_ubyte2_e32 v87, v26
	v_cvt_f32_ubyte3_e32 v88, v26
	v_fmac_f32_e32 v10, v85, v53
	v_fmac_f32_e32 v11, v86, v53
	v_fmac_f32_e32 v12, v87, v53
	v_fmac_f32_e32 v13, v88, v53
	v_cvt_f32_ubyte0_e32 v85, v27
	v_cvt_f32_ubyte1_e32 v86, v27
	v_cvt_f32_ubyte2_e32 v87, v27
	v_cvt_f32_ubyte3_e32 v88, v27
	v_fmac_f32_e32 v14, v85, v53
	v_fmac_f32_e32 v15, v86, v53
	v_fmac_f32_e32 v16, v87, v53
	v_fmac_f32_e32 v17, v88, v53
	v_add_f32_e32 v18, v18, v53
	s_waitcnt vmcnt(5)
	v_cvt_f32_ubyte0_e32 v85, v28
	v_cvt_f32_ubyte1_e32 v86, v28
	v_cvt_f32_ubyte2_e32 v87, v28
	v_cvt_f32_ubyte3_e32 v88, v28
	v_fmac_f32_e32 v2, v85, v54
	v_fmac_f32_e32 v3, v86, v54
	v_fmac_f32_e32 v4, v87, v54
	v_fmac_f32_e32 v5, v88, v54
	v_cvt_f32_ubyte0_e32 v85, v29
	v_cvt_f32_ubyte1_e32 v86, v29
	v_cvt_f32_ubyte2_e32 v87, v29
	v_cvt_f32_ubyte3_e32 v88, v29
	v_fmac_f32_e32 v6, v85, v54
	v_fmac_f32_e32 v7, v86, v54
	v_fmac_f32_e32 v8, v87, v54
	v_fmac_f32_e32 v9, v88, v54
	v_cvt_f32_ubyte0_e32 v85, v30
	v_cvt_f32_ubyte1_e32 v86, v30
	v_cvt_f32_ubyte2_e32 v87, v30
	v_cvt_f32_ubyte3_e32 v88, v30
	v_fmac_f32_e32 v10, v85, v54
	v_fmac_f32_e32 v11, v86, v54
	v_fmac_f32_e32 v12, v87, v54
	v_fmac_f32_e32 v13, v88, v54
	v_cvt_f32_ubyte0_e32 v85, v31
	v_cvt_f32_ubyte1_e32 v86, v31
	v_cvt_f32_ubyte2_e32 v87, v31
	v_cvt_f32_ubyte3_e32 v88, v31
	v_fmac_f32_e32 v14, v85, v54
	v_fmac_f32_e32 v15, v86, v54
	v_fmac_f32_e32 v16, v87, v54
	v_fmac_f32_e32 v17, v88, v54
	v_add_f32_e32 v18, v18, v54
	s_waitcnt vmcnt(4)
	v_cvt_f32_ubyte0_e32 v85, v32
	v_cvt_f32_ubyte1_e32 v86, v32
	v_cvt_f32_ubyte2_e32 v87, v32
	v_cvt_f32_ubyte3_e32 v88, v32
	v_fmac_f32_e32 v2, v85, v55
	v_fmac_f32_e32 v3, v86, v55
	v_fmac_f32_e32 v4, v87, v55
	v_fmac_f32_e32 v5, v88, v55
	v_cvt_f32_ubyte0_e32 v85, v33
	v_cvt_f32_ubyte1_e32 v86, v33
	v_cvt_f32_ubyte2_e32 v87, v33
	v_cvt_f32_ubyte3_e32 v88, v33
	v_fmac_f32_e32 v6, v85, v55
	v_fmac_f32_e32 v7, v86, v55
	v_fmac_f32_e32 v8, v87, v55
	v_fmac_f32_e32 v9, v88, v55
	v_cvt_f32_ubyte0_e32 v85, v34
	v_cvt_f32_ubyte1_e32 v86, v34
	v_cvt_f32_ubyte2_e32 v87, v34
	v_cvt_f32_ubyte3_e32 v88, v34
	v_fmac_f32_e32 v10, v85, v55
	v_fmac_f32_e32 v11, v86, v55
	v_fmac_f32_e32 v12, v87, v55
	v_fmac_f32_e32 v13, v88, v55
	v_cvt_f32_ubyte0_e32 v85, v35
	v_cvt_f32_ubyte1_e32 v86, v35
	v_cvt_f32_ubyte2_e32 v87, v35
	v_cvt_f32_ubyte3_e32 v88, v35
	v_fmac_f32_e32 v14, v85, v55
	v_fmac_f32_e32 v15, v86, v55
	v_fmac_f32_e32 v16, v87, v55
	v_fmac_f32_e32 v17, v88, v55
	v_add_f32_e32 v18, v18, v55
	s_waitcnt vmcnt(3)
	v_cvt_f32_ubyte0_e32 v85, v36
	v_cvt_f32_ubyte1_e32 v86, v36
	v_cvt_f32_ubyte2_e32 v87, v36
	v_cvt_f32_ubyte3_e32 v88, v36
	v_fmac_f32_e32 v2, v85, v56
	v_fmac_f32_e32 v3, v86, v56
	v_fmac_f32_e32 v4, v87, v56
	v_fmac_f32_e32 v5, v88, v56
	v_cvt_f32_ubyte0_e32 v85, v37
	v_cvt_f32_ubyte1_e32 v86, v37
	v_cvt_f32_ubyte2_e32 v87, v37
	v_cvt_f32_ubyte3_e32 v88, v37
	v_fmac_f32_e32 v6, v85, v56
	v_fmac_f32_e32 v7, v86, v56
	v_fmac_f32_e32 v8, v87, v56
	v_fmac_f32_e32 v9, v88, v56
	v_cvt_f32_ubyte0_e32 v85, v38
	v_cvt_f32_ubyte1_e32 v86, v38
	v_cvt_f32_ubyte2_e32 v87, v38
	v_cvt_f32_ubyte3_e32 v88, v38
	v_fmac_f32_e32 v10, v85, v56
	v_fmac_f32_e32 v11, v86, v56
	v_fmac_f32_e32 v12, v87, v56
	v_fmac_f32_e32 v13, v88, v56
	v_cvt_f32_ubyte0_e32 v85, v39
	v_cvt_f32_ubyte1_e32 v86, v39
	v_cvt_f32_ubyte2_e32 v87, v39
	v_cvt_f32_ubyte3_e32 v88, v39
	v_fmac_f32_e32 v14, v85, v56
	v_fmac_f32_e32 v15, v86, v56
	v_fmac_f32_e32 v16, v87, v56
	v_fmac_f32_e32 v17, v88, v56
	v_add_f32_e32 v18, v18, v56
	s_waitcnt vmcnt(2)
	v_cvt_f32_ubyte0_e32 v85, v40
	v_cvt_f32_ubyte1_e32 v86, v40
	v_cvt_f32_ubyte2_e32 v87, v40
	v_cvt_f32_ubyte3_e32 v88, v40
	v_fmac_f32_e32 v2, v85, v57
	v_fmac_f32_e32 v3, v86, v57
	v_fmac_f32_e32 v4, v87, v57
	v_fmac_f32_e32 v5, v88, v57
	v_cvt_f32_ubyte0_e32 v85, v41
	v_cvt_f32_ubyte1_e32 v86, v41
	v_cvt_f32_ubyte2_e32 v87, v41
	v_cvt_f32_ubyte3_e32 v88, v41
	v_fmac_f32_e32 v6, v85, v57
	v_fmac_f32_e32 v7, v86, v57
	v_fmac_f32_e32 v8, v87, v57
	v_fmac_f32_e32 v9, v88, v57
	v_cvt_f32_ubyte0_e32 v85, v42
	v_cvt_f32_ubyte1_e32 v86, v42
	v_cvt_f32_ubyte2_e32 v87, v42
	v_cvt_f32_ubyte3_e32 v88, v42
	v_fmac_f32_e32 v10, v85, v57
	v_fmac_f32_e32 v11, v86, v57
	v_fmac_f32_e32 v12, v87, v57
	v_fmac_f32_e32 v13, v88, v57
	v_cvt_f32_ubyte0_e32 v85, v43
	v_cvt_f32_ubyte1_e32 v86, v43
	v_cvt_f32_ubyte2_e32 v87, v43
	v_cvt_f32_ubyte3_e32 v88, v43
	v_fmac_f32_e32 v14, v85, v57
	v_fmac_f32_e32 v15, v86, v57
	v_fmac_f32_e32 v16, v87, v57
	v_fmac_f32_e32 v17, v88, v57
	v_add_f32_e32 v18, v18, v57
	s_waitcnt vmcnt(1)
	v_cvt_f32_ubyte0_e32 v85, v44
	v_cvt_f32_ubyte1_e32 v86, v44
	v_cvt_f32_ubyte2_e32 v87, v44
	v_cvt_f32_ubyte3_e32 v88, v44
	v_fmac_f32_e32 v2, v85, v58
	v_fmac_f32_e32 v3, v86, v58
	v_fmac_f32_e32 v4, v87, v58
	v_fmac_f32_e32 v5, v88, v58
	v_cvt_f32_ubyte0_e32 v85, v45
	v_cvt_f32_ubyte1_e32 v86, v45
	v_cvt_f32_ubyte2_e32 v87, v45
	v_cvt_f32_ubyte3_e32 v88, v45
	v_fmac_f32_e32 v6, v85, v58
	v_fmac_f32_e32 v7, v86, v58
	v_fmac_f32_e32 v8, v87, v58
	v_fmac_f32_e32 v9, v88, v58
	v_cvt_f32_ubyte0_e32 v85, v46
	v_cvt_f32_ubyte1_e32 v86, v46
	v_cvt_f32_ubyte2_e32 v87, v46
	v_cvt_f32_ubyte3_e32 v88, v46
	v_fmac_f32_e32 v10, v85, v58
	v_fmac_f32_e32 v11, v86, v58
	v_fmac_f32_e32 v12, v87, v58
	v_fmac_f32_e32 v13, v88, v58
	v_cvt_f32_ubyte0_e32 v85, v47
	v_cvt_f32_ubyte1_e32 v86, v47
	v_cvt_f32_ubyte2_e32 v87, v47
	v_cvt_f32_ubyte3_e32 v88, v47
	v_fmac_f32_e32 v14, v85, v58
	v_fmac_f32_e32 v15, v86, v58
	v_fmac_f32_e32 v16, v87, v58
	v_fmac_f32_e32 v17, v88, v58
	v_add_f32_e32 v18, v18, v58
	s_waitcnt vmcnt(0)
	v_cvt_f32_ubyte0_e32 v85, v48
	v_cvt_f32_ubyte1_e32 v86, v48
	v_cvt_f32_ubyte2_e32 v87, v48
	v_cvt_f32_ubyte3_e32 v88, v48
	v_fmac_f32_e32 v2, v85, v59
	v_fmac_f32_e32 v3, v86, v59
	v_fmac_f32_e32 v4, v87, v59
	v_fmac_f32_e32 v5, v88, v59
	v_cvt_f32_ubyte0_e32 v85, v49
	v_cvt_f32_ubyte1_e32 v86, v49
	v_cvt_f32_ubyte2_e32 v87, v49
	v_cvt_f32_ubyte3_e32 v88, v49
	v_fmac_f32_e32 v6, v85, v59
	v_fmac_f32_e32 v7, v86, v59
	v_fmac_f32_e32 v8, v87, v59
	v_fmac_f32_e32 v9, v88, v59
	v_cvt_f32_ubyte0_e32 v85, v50
	v_cvt_f32_ubyte1_e32 v86, v50
	v_cvt_f32_ubyte2_e32 v87, v50
	v_cvt_f32_ubyte3_e32 v88, v50
	v_fmac_f32_e32 v10, v85, v59
	v_fmac_f32_e32 v11, v86, v59
	v_fmac_f32_e32 v12, v87, v59
	v_fmac_f32_e32 v13, v88, v59
	v_cvt_f32_ubyte0_e32 v85, v51
	v_cvt_f32_ubyte1_e32 v86, v51
	v_cvt_f32_ubyte2_e32 v87, v51
	v_cvt_f32_ubyte3_e32 v88, v51
	v_fmac_f32_e32 v14, v85, v59
	v_fmac_f32_e32 v15, v86, v59
	v_fmac_f32_e32 v16, v87, v59
	v_fmac_f32_e32 v17, v88, v59
	v_add_f32_e32 v18, v18, v59
	s_branch .Lg1_rare_check
.Lg1_tailb0:
	s_waitcnt vmcnt(7)
	v_cvt_f32_ubyte0_e32 v85, v20
	v_cvt_f32_ubyte1_e32 v86, v20
	v_cvt_f32_ubyte2_e32 v87, v20
	v_cvt_f32_ubyte3_e32 v88, v20
	v_fmac_f32_e32 v2, v85, v52
	v_fmac_f32_e32 v3, v86, v52
	v_fmac_f32_e32 v4, v87, v52
	v_fmac_f32_e32 v5, v88, v52
	v_cvt_f32_ubyte0_e32 v85, v21
	v_cvt_f32_ubyte1_e32 v86, v21
	v_cvt_f32_ubyte2_e32 v87, v21
	v_cvt_f32_ubyte3_e32 v88, v21
	v_fmac_f32_e32 v6, v85, v52
	v_fmac_f32_e32 v7, v86, v52
	v_fmac_f32_e32 v8, v87, v52
	v_fmac_f32_e32 v9, v88, v52
	v_cvt_f32_ubyte0_e32 v85, v22
	v_cvt_f32_ubyte1_e32 v86, v22
	v_cvt_f32_ubyte2_e32 v87, v22
	v_cvt_f32_ubyte3_e32 v88, v22
	v_fmac_f32_e32 v10, v85, v52
	v_fmac_f32_e32 v11, v86, v52
	v_fmac_f32_e32 v12, v87, v52
	v_fmac_f32_e32 v13, v88, v52
	v_cvt_f32_ubyte0_e32 v85, v23
	v_cvt_f32_ubyte1_e32 v86, v23
	v_cvt_f32_ubyte2_e32 v87, v23
	v_cvt_f32_ubyte3_e32 v88, v23
	v_fmac_f32_e32 v14, v85, v52
	v_fmac_f32_e32 v15, v86, v52
	v_fmac_f32_e32 v16, v87, v52
	v_fmac_f32_e32 v17, v88, v52
	v_add_f32_e32 v18, v18, v52
	global_load_dwordx4 v[20:23], v103, s[8:9] offset:0
	s_waitcnt vmcnt(7)
	v_cvt_f32_ubyte0_e32 v85, v24
	v_cvt_f32_ubyte1_e32 v86, v24
	v_cvt_f32_ubyte2_e32 v87, v24
	v_cvt_f32_ubyte3_e32 v88, v24
	v_fmac_f32_e32 v2, v85, v53
	v_fmac_f32_e32 v3, v86, v53
	v_fmac_f32_e32 v4, v87, v53
	v_fmac_f32_e32 v5, v88, v53
	v_cvt_f32_ubyte0_e32 v85, v25
	v_cvt_f32_ubyte1_e32 v86, v25
	v_cvt_f32_ubyte2_e32 v87, v25
	v_cvt_f32_ubyte3_e32 v88, v25
	v_fmac_f32_e32 v6, v85, v53
	v_fmac_f32_e32 v7, v86, v53
	v_fmac_f32_e32 v8, v87, v53
	v_fmac_f32_e32 v9, v88, v53
	v_cvt_f32_ubyte0_e32 v85, v26
	v_cvt_f32_ubyte1_e32 v86, v26
	v_cvt_f32_ubyte2_e32 v87, v26
	v_cvt_f32_ubyte3_e32 v88, v26
	v_fmac_f32_e32 v10, v85, v53
	v_fmac_f32_e32 v11, v86, v53
	v_fmac_f32_e32 v12, v87, v53
	v_fmac_f32_e32 v13, v88, v53
	v_cvt_f32_ubyte0_e32 v85, v27
	v_cvt_f32_ubyte1_e32 v86, v27
	v_cvt_f32_ubyte2_e32 v87, v27
	v_cvt_f32_ubyte3_e32 v88, v27
	v_fmac_f32_e32 v14, v85, v53
	v_fmac_f32_e32 v15, v86, v53
	v_fmac_f32_e32 v16, v87, v53
	v_fmac_f32_e32 v17, v88, v53
	v_add_f32_e32 v18, v18, v53
	global_load_dwordx4 v[24:27], v103, s[8:9] offset:16
	s_waitcnt vmcnt(7)
	v_cvt_f32_ubyte0_e32 v85, v28
	v_cvt_f32_ubyte1_e32 v86, v28
	v_cvt_f32_ubyte2_e32 v87, v28
	v_cvt_f32_ubyte3_e32 v88, v28
	v_fmac_f32_e32 v2, v85, v54
	v_fmac_f32_e32 v3, v86, v54
	v_fmac_f32_e32 v4, v87, v54
	v_fmac_f32_e32 v5, v88, v54
	v_cvt_f32_ubyte0_e32 v85, v29
	v_cvt_f32_ubyte1_e32 v86, v29
	v_cvt_f32_ubyte2_e32 v87, v29
	v_cvt_f32_ubyte3_e32 v88, v29
	v_fmac_f32_e32 v6, v85, v54
	v_fmac_f32_e32 v7, v86, v54
	v_fmac_f32_e32 v8, v87, v54
	v_fmac_f32_e32 v9, v88, v54
	v_cvt_f32_ubyte0_e32 v85, v30
	v_cvt_f32_ubyte1_e32 v86, v30
	v_cvt_f32_ubyte2_e32 v87, v30
	v_cvt_f32_ubyte3_e32 v88, v30
	v_fmac_f32_e32 v10, v85, v54
	v_fmac_f32_e32 v11, v86, v54
	v_fmac_f32_e32 v12, v87, v54
	v_fmac_f32_e32 v13, v88, v54
	v_cvt_f32_ubyte0_e32 v85, v31
	v_cvt_f32_ubyte1_e32 v86, v31
	v_cvt_f32_ubyte2_e32 v87, v31
	v_cvt_f32_ubyte3_e32 v88, v31
	v_fmac_f32_e32 v14, v85, v54
	v_fmac_f32_e32 v15, v86, v54
	v_fmac_f32_e32 v16, v87, v54
	v_fmac_f32_e32 v17, v88, v54
	v_add_f32_e32 v18, v18, v54
	global_load_dwordx4 v[28:31], v103, s[8:9] offset:128
	s_waitcnt vmcnt(7)
	v_cvt_f32_ubyte0_e32 v85, v32
	v_cvt_f32_ubyte1_e32 v86, v32
	v_cvt_f32_ubyte2_e32 v87, v32
	v_cvt_f32_ubyte3_e32 v88, v32
	v_fmac_f32_e32 v2, v85, v55
	v_fmac_f32_e32 v3, v86, v55
	v_fmac_f32_e32 v4, v87, v55
	v_fmac_f32_e32 v5, v88, v55
	v_cvt_f32_ubyte0_e32 v85, v33
	v_cvt_f32_ubyte1_e32 v86, v33
	v_cvt_f32_ubyte2_e32 v87, v33
	v_cvt_f32_ubyte3_e32 v88, v33
	v_fmac_f32_e32 v6, v85, v55
	v_fmac_f32_e32 v7, v86, v55
	v_fmac_f32_e32 v8, v87, v55
	v_fmac_f32_e32 v9, v88, v55
	v_cvt_f32_ubyte0_e32 v85, v34
	v_cvt_f32_ubyte1_e32 v86, v34
	v_cvt_f32_ubyte2_e32 v87, v34
	v_cvt_f32_ubyte3_e32 v88, v34
	v_fmac_f32_e32 v10, v85, v55
	v_fmac_f32_e32 v11, v86, v55
	v_fmac_f32_e32 v12, v87, v55
	v_fmac_f32_e32 v13, v88, v55
	v_cvt_f32_ubyte0_e32 v85, v35
	v_cvt_f32_ubyte1_e32 v86, v35
	v_cvt_f32_ubyte2_e32 v87, v35
	v_cvt_f32_ubyte3_e32 v88, v35
	v_fmac_f32_e32 v14, v85, v55
	v_fmac_f32_e32 v15, v86, v55
	v_fmac_f32_e32 v16, v87, v55
	v_fmac_f32_e32 v17, v88, v55
	v_add_f32_e32 v18, v18, v55
	global_load_dwordx4 v[32:35], v103, s[8:9] offset:144
	s_waitcnt vmcnt(7)
	v_cvt_f32_ubyte0_e32 v85, v36
	v_cvt_f32_ubyte1_e32 v86, v36
	v_cvt_f32_ubyte2_e32 v87, v36
	v_cvt_f32_ubyte3_e32 v88, v36
	v_fmac_f32_e32 v2, v85, v56
	v_fmac_f32_e32 v3, v86, v56
	v_fmac_f32_e32 v4, v87, v56
	v_fmac_f32_e32 v5, v88, v56
	v_cvt_f32_ubyte0_e32 v85, v37
	v_cvt_f32_ubyte1_e32 v86, v37
	v_cvt_f32_ubyte2_e32 v87, v37
	v_cvt_f32_ubyte3_e32 v88, v37
	v_fmac_f32_e32 v6, v85, v56
	v_fmac_f32_e32 v7, v86, v56
	v_fmac_f32_e32 v8, v87, v56
	v_fmac_f32_e32 v9, v88, v56
	v_cvt_f32_ubyte0_e32 v85, v38
	v_cvt_f32_ubyte1_e32 v86, v38
	v_cvt_f32_ubyte2_e32 v87, v38
	v_cvt_f32_ubyte3_e32 v88, v38
	v_fmac_f32_e32 v10, v85, v56
	v_fmac_f32_e32 v11, v86, v56
	v_fmac_f32_e32 v12, v87, v56
	v_fmac_f32_e32 v13, v88, v56
	v_cvt_f32_ubyte0_e32 v85, v39
	v_cvt_f32_ubyte1_e32 v86, v39
	v_cvt_f32_ubyte2_e32 v87, v39
	v_cvt_f32_ubyte3_e32 v88, v39
	v_fmac_f32_e32 v14, v85, v56
	v_fmac_f32_e32 v15, v86, v56
	v_fmac_f32_e32 v16, v87, v56
	v_fmac_f32_e32 v17, v88, v56
	v_add_f32_e32 v18, v18, v56
	global_load_dwordx4 v[36:39], v103, s[8:9] offset:256
	s_waitcnt vmcnt(7)
	v_cvt_f32_ubyte0_e32 v85, v40
	v_cvt_f32_ubyte1_e32 v86, v40
	v_cvt_f32_ubyte2_e32 v87, v40
	v_cvt_f32_ubyte3_e32 v88, v40
	v_fmac_f32_e32 v2, v85, v57
	v_fmac_f32_e32 v3, v86, v57
	v_fmac_f32_e32 v4, v87, v57
	v_fmac_f32_e32 v5, v88, v57
	v_cvt_f32_ubyte0_e32 v85, v41
	v_cvt_f32_ubyte1_e32 v86, v41
	v_cvt_f32_ubyte2_e32 v87, v41
	v_cvt_f32_ubyte3_e32 v88, v41
	v_fmac_f32_e32 v6, v85, v57
	v_fmac_f32_e32 v7, v86, v57
	v_fmac_f32_e32 v8, v87, v57
	v_fmac_f32_e32 v9, v88, v57
	v_cvt_f32_ubyte0_e32 v85, v42
	v_cvt_f32_ubyte1_e32 v86, v42
	v_cvt_f32_ubyte2_e32 v87, v42
	v_cvt_f32_ubyte3_e32 v88, v42
	v_fmac_f32_e32 v10, v85, v57
	v_fmac_f32_e32 v11, v86, v57
	v_fmac_f32_e32 v12, v87, v57
	v_fmac_f32_e32 v13, v88, v57
	v_cvt_f32_ubyte0_e32 v85, v43
	v_cvt_f32_ubyte1_e32 v86, v43
	v_cvt_f32_ubyte2_e32 v87, v43
	v_cvt_f32_ubyte3_e32 v88, v43
	v_fmac_f32_e32 v14, v85, v57
	v_fmac_f32_e32 v15, v86, v57
	v_fmac_f32_e32 v16, v87, v57
	v_fmac_f32_e32 v17, v88, v57
	v_add_f32_e32 v18, v18, v57
	global_load_dwordx4 v[40:43], v103, s[8:9] offset:272
	s_waitcnt vmcnt(7)
	v_cvt_f32_ubyte0_e32 v85, v44
	v_cvt_f32_ubyte1_e32 v86, v44
	v_cvt_f32_ubyte2_e32 v87, v44
	v_cvt_f32_ubyte3_e32 v88, v44
	v_fmac_f32_e32 v2, v85, v58
	v_fmac_f32_e32 v3, v86, v58
	v_fmac_f32_e32 v4, v87, v58
	v_fmac_f32_e32 v5, v88, v58
	v_cvt_f32_ubyte0_e32 v85, v45
	v_cvt_f32_ubyte1_e32 v86, v45
	v_cvt_f32_ubyte2_e32 v87, v45
	v_cvt_f32_ubyte3_e32 v88, v45
	v_fmac_f32_e32 v6, v85, v58
	v_fmac_f32_e32 v7, v86, v58
	v_fmac_f32_e32 v8, v87, v58
	v_fmac_f32_e32 v9, v88, v58
	v_cvt_f32_ubyte0_e32 v85, v46
	v_cvt_f32_ubyte1_e32 v86, v46
	v_cvt_f32_ubyte2_e32 v87, v46
	v_cvt_f32_ubyte3_e32 v88, v46
	v_fmac_f32_e32 v10, v85, v58
	v_fmac_f32_e32 v11, v86, v58
	v_fmac_f32_e32 v12, v87, v58
	v_fmac_f32_e32 v13, v88, v58
	v_cvt_f32_ubyte0_e32 v85, v47
	v_cvt_f32_ubyte1_e32 v86, v47
	v_cvt_f32_ubyte2_e32 v87, v47
	v_cvt_f32_ubyte3_e32 v88, v47
	v_fmac_f32_e32 v14, v85, v58
	v_fmac_f32_e32 v15, v86, v58
	v_fmac_f32_e32 v16, v87, v58
	v_fmac_f32_e32 v17, v88, v58
	v_add_f32_e32 v18, v18, v58
	global_load_dwordx4 v[44:47], v103, s[8:9] offset:384
	s_waitcnt vmcnt(7)
	v_cvt_f32_ubyte0_e32 v85, v48
	v_cvt_f32_ubyte1_e32 v86, v48
	v_cvt_f32_ubyte2_e32 v87, v48
	v_cvt_f32_ubyte3_e32 v88, v48
	v_fmac_f32_e32 v2, v85, v59
	v_fmac_f32_e32 v3, v86, v59
	v_fmac_f32_e32 v4, v87, v59
	v_fmac_f32_e32 v5, v88, v59
	v_cvt_f32_ubyte0_e32 v85, v49
	v_cvt_f32_ubyte1_e32 v86, v49
	v_cvt_f32_ubyte2_e32 v87, v49
	v_cvt_f32_ubyte3_e32 v88, v49
	v_fmac_f32_e32 v6, v85, v59
	v_fmac_f32_e32 v7, v86, v59
	v_fmac_f32_e32 v8, v87, v59
	v_fmac_f32_e32 v9, v88, v59
	v_cvt_f32_ubyte0_e32 v85, v50
	v_cvt_f32_ubyte1_e32 v86, v50
	v_cvt_f32_ubyte2_e32 v87, v50
	v_cvt_f32_ubyte3_e32 v88, v50
	v_fmac_f32_e32 v10, v85, v59
	v_fmac_f32_e32 v11, v86, v59
	v_fmac_f32_e32 v12, v87, v59
	v_fmac_f32_e32 v13, v88, v59
	v_cvt_f32_ubyte0_e32 v85, v51
	v_cvt_f32_ubyte1_e32 v86, v51
	v_cvt_f32_ubyte2_e32 v87, v51
	v_cvt_f32_ubyte3_e32 v88, v51
	v_fmac_f32_e32 v14, v85, v59
	v_fmac_f32_e32 v15, v86, v59
	v_fmac_f32_e32 v16, v87, v59
	v_fmac_f32_e32 v17, v88, v59
	v_add_f32_e32 v18, v18, v59
	global_load_dwordx4 v[48:51], v103, s[8:9] offset:400
	s_branch .Lg1_rare_check
.Lg1_tail4:
	s_cmp_eq_u32 s39, 1
	s_cbranch_scc1 .Lg1_tailb4
	s_waitcnt vmcnt(7)
	v_cvt_f32_ubyte0_e32 v85, v36
	v_cvt_f32_ubyte1_e32 v86, v36
	v_cvt_f32_ubyte2_e32 v87, v36
	v_cvt_f32_ubyte3_e32 v88, v36
	v_fmac_f32_e32 v2, v85, v56
	v_fmac_f32_e32 v3, v86, v56
	v_fmac_f32_e32 v4, v87, v56
	v_fmac_f32_e32 v5, v88, v56
	v_cvt_f32_ubyte0_e32 v85, v37
	v_cvt_f32_ubyte1_e32 v86, v37
	v_cvt_f32_ubyte2_e32 v87, v37
	v_cvt_f32_ubyte3_e32 v88, v37
	v_fmac_f32_e32 v6, v85, v56
	v_fmac_f32_e32 v7, v86, v56
	v_fmac_f32_e32 v8, v87, v56
	v_fmac_f32_e32 v9, v88, v56
	v_cvt_f32_ubyte0_e32 v85, v38
	v_cvt_f32_ubyte1_e32 v86, v38
	v_cvt_f32_ubyte2_e32 v87, v38
	v_cvt_f32_ubyte3_e32 v88, v38
	v_fmac_f32_e32 v10, v85, v56
	v_fmac_f32_e32 v11, v86, v56
	v_fmac_f32_e32 v12, v87, v56
	v_fmac_f32_e32 v13, v88, v56
	v_cvt_f32_ubyte0_e32 v85, v39
	v_cvt_f32_ubyte1_e32 v86, v39
	v_cvt_f32_ubyte2_e32 v87, v39
	v_cvt_f32_ubyte3_e32 v88, v39
	v_fmac_f32_e32 v14, v85, v56
	v_fmac_f32_e32 v15, v86, v56
	v_fmac_f32_e32 v16, v87, v56
	v_fmac_f32_e32 v17, v88, v56
	v_add_f32_e32 v18, v18, v56
	s_waitcnt vmcnt(6)
	v_cvt_f32_ubyte0_e32 v85, v40
	v_cvt_f32_ubyte1_e32 v86, v40
	v_cvt_f32_ubyte2_e32 v87, v40
	v_cvt_f32_ubyte3_e32 v88, v40
	v_fmac_f32_e32 v2, v85, v57
	v_fmac_f32_e32 v3, v86, v57
	v_fmac_f32_e32 v4, v87, v57
	v_fmac_f32_e32 v5, v88, v57
	v_cvt_f32_ubyte0_e32 v85, v41
	v_cvt_f32_ubyte1_e32 v86, v41
	v_cvt_f32_ubyte2_e32 v87, v41
	v_cvt_f32_ubyte3_e32 v88, v41
	v_fmac_f32_e32 v6, v85, v57
	v_fmac_f32_e32 v7, v86, v57
	v_fmac_f32_e32 v8, v87, v57
	v_fmac_f32_e32 v9, v88, v57
	v_cvt_f32_ubyte0_e32 v85, v42
	v_cvt_f32_ubyte1_e32 v86, v42
	v_cvt_f32_ubyte2_e32 v87, v42
	v_cvt_f32_ubyte3_e32 v88, v42
	v_fmac_f32_e32 v10, v85, v57
	v_fmac_f32_e32 v11, v86, v57
	v_fmac_f32_e32 v12, v87, v57
	v_fmac_f32_e32 v13, v88, v57
	v_cvt_f32_ubyte0_e32 v85, v43
	v_cvt_f32_ubyte1_e32 v86, v43
	v_cvt_f32_ubyte2_e32 v87, v43
	v_cvt_f32_ubyte3_e32 v88, v43
	v_fmac_f32_e32 v14, v85, v57
	v_fmac_f32_e32 v15, v86, v57
	v_fmac_f32_e32 v16, v87, v57
	v_fmac_f32_e32 v17, v88, v57
	v_add_f32_e32 v18, v18, v57
	s_waitcnt vmcnt(5)
	v_cvt_f32_ubyte0_e32 v85, v44
	v_cvt_f32_ubyte1_e32 v86, v44
	v_cvt_f32_ubyte2_e32 v87, v44
	v_cvt_f32_ubyte3_e32 v88, v44
	v_fmac_f32_e32 v2, v85, v58
	v_fmac_f32_e32 v3, v86, v58
	v_fmac_f32_e32 v4, v87, v58
	v_fmac_f32_e32 v5, v88, v58
	v_cvt_f32_ubyte0_e32 v85, v45
	v_cvt_f32_ubyte1_e32 v86, v45
	v_cvt_f32_ubyte2_e32 v87, v45
	v_cvt_f32_ubyte3_e32 v88, v45
	v_fmac_f32_e32 v6, v85, v58
	v_fmac_f32_e32 v7, v86, v58
	v_fmac_f32_e32 v8, v87, v58
	v_fmac_f32_e32 v9, v88, v58
	v_cvt_f32_ubyte0_e32 v85, v46
	v_cvt_f32_ubyte1_e32 v86, v46
	v_cvt_f32_ubyte2_e32 v87, v46
	v_cvt_f32_ubyte3_e32 v88, v46
	v_fmac_f32_e32 v10, v85, v58
	v_fmac_f32_e32 v11, v86, v58
	v_fmac_f32_e32 v12, v87, v58
	v_fmac_f32_e32 v13, v88, v58
	v_cvt_f32_ubyte0_e32 v85, v47
	v_cvt_f32_ubyte1_e32 v86, v47
	v_cvt_f32_ubyte2_e32 v87, v47
	v_cvt_f32_ubyte3_e32 v88, v47
	v_fmac_f32_e32 v14, v85, v58
	v_fmac_f32_e32 v15, v86, v58
	v_fmac_f32_e32 v16, v87, v58
	v_fmac_f32_e32 v17, v88, v58
	v_add_f32_e32 v18, v18, v58
	s_waitcnt vmcnt(4)
	v_cvt_f32_ubyte0_e32 v85, v48
	v_cvt_f32_ubyte1_e32 v86, v48
	v_cvt_f32_ubyte2_e32 v87, v48
	v_cvt_f32_ubyte3_e32 v88, v48
	v_fmac_f32_e32 v2, v85, v59
	v_fmac_f32_e32 v3, v86, v59
	v_fmac_f32_e32 v4, v87, v59
	v_fmac_f32_e32 v5, v88, v59
	v_cvt_f32_ubyte0_e32 v85, v49
	v_cvt_f32_ubyte1_e32 v86, v49
	v_cvt_f32_ubyte2_e32 v87, v49
	v_cvt_f32_ubyte3_e32 v88, v49
	v_fmac_f32_e32 v6, v85, v59
	v_fmac_f32_e32 v7, v86, v59
	v_fmac_f32_e32 v8, v87, v59
	v_fmac_f32_e32 v9, v88, v59
	v_cvt_f32_ubyte0_e32 v85, v50
	v_cvt_f32_ubyte1_e32 v86, v50
	v_cvt_f32_ubyte2_e32 v87, v50
	v_cvt_f32_ubyte3_e32 v88, v50
	v_fmac_f32_e32 v10, v85, v59
	v_fmac_f32_e32 v11, v86, v59
	v_fmac_f32_e32 v12, v87, v59
	v_fmac_f32_e32 v13, v88, v59
	v_cvt_f32_ubyte0_e32 v85, v51
	v_cvt_f32_ubyte1_e32 v86, v51
	v_cvt_f32_ubyte2_e32 v87, v51
	v_cvt_f32_ubyte3_e32 v88, v51
	v_fmac_f32_e32 v14, v85, v59
	v_fmac_f32_e32 v15, v86, v59
	v_fmac_f32_e32 v16, v87, v59
	v_fmac_f32_e32 v17, v88, v59
	v_add_f32_e32 v18, v18, v59
	s_waitcnt vmcnt(3)
	v_cvt_f32_ubyte0_e32 v85, v20
	v_cvt_f32_ubyte1_e32 v86, v20
	v_cvt_f32_ubyte2_e32 v87, v20
	v_cvt_f32_ubyte3_e32 v88, v20
	v_fmac_f32_e32 v2, v85, v52
	v_fmac_f32_e32 v3, v86, v52
	v_fmac_f32_e32 v4, v87, v52
	v_fmac_f32_e32 v5, v88, v52
	v_cvt_f32_ubyte0_e32 v85, v21
	v_cvt_f32_ubyte1_e32 v86, v21
	v_cvt_f32_ubyte2_e32 v87, v21
	v_cvt_f32_ubyte3_e32 v88, v21
	v_fmac_f32_e32 v6, v85, v52
	v_fmac_f32_e32 v7, v86, v52
	v_fmac_f32_e32 v8, v87, v52
	v_fmac_f32_e32 v9, v88, v52
	v_cvt_f32_ubyte0_e32 v85, v22
	v_cvt_f32_ubyte1_e32 v86, v22
	v_cvt_f32_ubyte2_e32 v87, v22
	v_cvt_f32_ubyte3_e32 v88, v22
	v_fmac_f32_e32 v10, v85, v52
	v_fmac_f32_e32 v11, v86, v52
	v_fmac_f32_e32 v12, v87, v52
	v_fmac_f32_e32 v13, v88, v52
	v_cvt_f32_ubyte0_e32 v85, v23
	v_cvt_f32_ubyte1_e32 v86, v23
	v_cvt_f32_ubyte2_e32 v87, v23
	v_cvt_f32_ubyte3_e32 v88, v23
	v_fmac_f32_e32 v14, v85, v52
	v_fmac_f32_e32 v15, v86, v52
	v_fmac_f32_e32 v16, v87, v52
	v_fmac_f32_e32 v17, v88, v52
	v_add_f32_e32 v18, v18, v52
	s_waitcnt vmcnt(2)
	v_cvt_f32_ubyte0_e32 v85, v24
	v_cvt_f32_ubyte1_e32 v86, v24
	v_cvt_f32_ubyte2_e32 v87, v24
	v_cvt_f32_ubyte3_e32 v88, v24
	v_fmac_f32_e32 v2, v85, v53
	v_fmac_f32_e32 v3, v86, v53
	v_fmac_f32_e32 v4, v87, v53
	v_fmac_f32_e32 v5, v88, v53
	v_cvt_f32_ubyte0_e32 v85, v25
	v_cvt_f32_ubyte1_e32 v86, v25
	v_cvt_f32_ubyte2_e32 v87, v25
	v_cvt_f32_ubyte3_e32 v88, v25
	v_fmac_f32_e32 v6, v85, v53
	v_fmac_f32_e32 v7, v86, v53
	v_fmac_f32_e32 v8, v87, v53
	v_fmac_f32_e32 v9, v88, v53
	v_cvt_f32_ubyte0_e32 v85, v26
	v_cvt_f32_ubyte1_e32 v86, v26
	v_cvt_f32_ubyte2_e32 v87, v26
	v_cvt_f32_ubyte3_e32 v88, v26
	v_fmac_f32_e32 v10, v85, v53
	v_fmac_f32_e32 v11, v86, v53
	v_fmac_f32_e32 v12, v87, v53
	v_fmac_f32_e32 v13, v88, v53
	v_cvt_f32_ubyte0_e32 v85, v27
	v_cvt_f32_ubyte1_e32 v86, v27
	v_cvt_f32_ubyte2_e32 v87, v27
	v_cvt_f32_ubyte3_e32 v88, v27
	v_fmac_f32_e32 v14, v85, v53
	v_fmac_f32_e32 v15, v86, v53
	v_fmac_f32_e32 v16, v87, v53
	v_fmac_f32_e32 v17, v88, v53
	v_add_f32_e32 v18, v18, v53
	s_waitcnt vmcnt(1)
	v_cvt_f32_ubyte0_e32 v85, v28
	v_cvt_f32_ubyte1_e32 v86, v28
	v_cvt_f32_ubyte2_e32 v87, v28
	v_cvt_f32_ubyte3_e32 v88, v28
	v_fmac_f32_e32 v2, v85, v54
	v_fmac_f32_e32 v3, v86, v54
	v_fmac_f32_e32 v4, v87, v54
	v_fmac_f32_e32 v5, v88, v54
	v_cvt_f32_ubyte0_e32 v85, v29
	v_cvt_f32_ubyte1_e32 v86, v29
	v_cvt_f32_ubyte2_e32 v87, v29
	v_cvt_f32_ubyte3_e32 v88, v29
	v_fmac_f32_e32 v6, v85, v54
	v_fmac_f32_e32 v7, v86, v54
	v_fmac_f32_e32 v8, v87, v54
	v_fmac_f32_e32 v9, v88, v54
	v_cvt_f32_ubyte0_e32 v85, v30
	v_cvt_f32_ubyte1_e32 v86, v30
	v_cvt_f32_ubyte2_e32 v87, v30
	v_cvt_f32_ubyte3_e32 v88, v30
	v_fmac_f32_e32 v10, v85, v54
	v_fmac_f32_e32 v11, v86, v54
	v_fmac_f32_e32 v12, v87, v54
	v_fmac_f32_e32 v13, v88, v54
	v_cvt_f32_ubyte0_e32 v85, v31
	v_cvt_f32_ubyte1_e32 v86, v31
	v_cvt_f32_ubyte2_e32 v87, v31
	v_cvt_f32_ubyte3_e32 v88, v31
	v_fmac_f32_e32 v14, v85, v54
	v_fmac_f32_e32 v15, v86, v54
	v_fmac_f32_e32 v16, v87, v54
	v_fmac_f32_e32 v17, v88, v54
	v_add_f32_e32 v18, v18, v54
	s_waitcnt vmcnt(0)
	v_cvt_f32_ubyte0_e32 v85, v32
	v_cvt_f32_ubyte1_e32 v86, v32
	v_cvt_f32_ubyte2_e32 v87, v32
	v_cvt_f32_ubyte3_e32 v88, v32
	v_fmac_f32_e32 v2, v85, v55
	v_fmac_f32_e32 v3, v86, v55
	v_fmac_f32_e32 v4, v87, v55
	v_fmac_f32_e32 v5, v88, v55
	v_cvt_f32_ubyte0_e32 v85, v33
	v_cvt_f32_ubyte1_e32 v86, v33
	v_cvt_f32_ubyte2_e32 v87, v33
	v_cvt_f32_ubyte3_e32 v88, v33
	v_fmac_f32_e32 v6, v85, v55
	v_fmac_f32_e32 v7, v86, v55
	v_fmac_f32_e32 v8, v87, v55
	v_fmac_f32_e32 v9, v88, v55
	v_cvt_f32_ubyte0_e32 v85, v34
	v_cvt_f32_ubyte1_e32 v86, v34
	v_cvt_f32_ubyte2_e32 v87, v34
	v_cvt_f32_ubyte3_e32 v88, v34
	v_fmac_f32_e32 v10, v85, v55
	v_fmac_f32_e32 v11, v86, v55
	v_fmac_f32_e32 v12, v87, v55
	v_fmac_f32_e32 v13, v88, v55
	v_cvt_f32_ubyte0_e32 v85, v35
	v_cvt_f32_ubyte1_e32 v86, v35
	v_cvt_f32_ubyte2_e32 v87, v35
	v_cvt_f32_ubyte3_e32 v88, v35
	v_fmac_f32_e32 v14, v85, v55
	v_fmac_f32_e32 v15, v86, v55
	v_fmac_f32_e32 v16, v87, v55
	v_fmac_f32_e32 v17, v88, v55
	v_add_f32_e32 v18, v18, v55
	s_branch .Lg1_rare_check
.Lg1_tailb4:
	s_waitcnt vmcnt(7)
	v_cvt_f32_ubyte0_e32 v85, v36
	v_cvt_f32_ubyte1_e32 v86, v36
	v_cvt_f32_ubyte2_e32 v87, v36
	v_cvt_f32_ubyte3_e32 v88, v36
	v_fmac_f32_e32 v2, v85, v56
	v_fmac_f32_e32 v3, v86, v56
	v_fmac_f32_e32 v4, v87, v56
	v_fmac_f32_e32 v5, v88, v56
	v_cvt_f32_ubyte0_e32 v85, v37
	v_cvt_f32_ubyte1_e32 v86, v37
	v_cvt_f32_ubyte2_e32 v87, v37
	v_cvt_f32_ubyte3_e32 v88, v37
	v_fmac_f32_e32 v6, v85, v56
	v_fmac_f32_e32 v7, v86, v56
	v_fmac_f32_e32 v8, v87, v56
	v_fmac_f32_e32 v9, v88, v56
	v_cvt_f32_ubyte0_e32 v85, v38
	v_cvt_f32_ubyte1_e32 v86, v38
	v_cvt_f32_ubyte2_e32 v87, v38
	v_cvt_f32_ubyte3_e32 v88, v38
	v_fmac_f32_e32 v10, v85, v56
	v_fmac_f32_e32 v11, v86, v56
	v_fmac_f32_e32 v12, v87, v56
	v_fmac_f32_e32 v13, v88, v56
	v_cvt_f32_ubyte0_e32 v85, v39
	v_cvt_f32_ubyte1_e32 v86, v39
	v_cvt_f32_ubyte2_e32 v87, v39
	v_cvt_f32_ubyte3_e32 v88, v39
	v_fmac_f32_e32 v14, v85, v56
	v_fmac_f32_e32 v15, v86, v56
	v_fmac_f32_e32 v16, v87, v56
	v_fmac_f32_e32 v17, v88, v56
	v_add_f32_e32 v18, v18, v56
	global_load_dwordx4 v[36:39], v103, s[8:9] offset:256
	s_waitcnt vmcnt(7)
	v_cvt_f32_ubyte0_e32 v85, v40
	v_cvt_f32_ubyte1_e32 v86, v40
	v_cvt_f32_ubyte2_e32 v87, v40
	v_cvt_f32_ubyte3_e32 v88, v40
	v_fmac_f32_e32 v2, v85, v57
	v_fmac_f32_e32 v3, v86, v57
	v_fmac_f32_e32 v4, v87, v57
	v_fmac_f32_e32 v5, v88, v57
	v_cvt_f32_ubyte0_e32 v85, v41
	v_cvt_f32_ubyte1_e32 v86, v41
	v_cvt_f32_ubyte2_e32 v87, v41
	v_cvt_f32_ubyte3_e32 v88, v41
	v_fmac_f32_e32 v6, v85, v57
	v_fmac_f32_e32 v7, v86, v57
	v_fmac_f32_e32 v8, v87, v57
	v_fmac_f32_e32 v9, v88, v57
	v_cvt_f32_ubyte0_e32 v85, v42
	v_cvt_f32_ubyte1_e32 v86, v42
	v_cvt_f32_ubyte2_e32 v87, v42
	v_cvt_f32_ubyte3_e32 v88, v42
	v_fmac_f32_e32 v10, v85, v57
	v_fmac_f32_e32 v11, v86, v57
	v_fmac_f32_e32 v12, v87, v57
	v_fmac_f32_e32 v13, v88, v57
	v_cvt_f32_ubyte0_e32 v85, v43
	v_cvt_f32_ubyte1_e32 v86, v43
	v_cvt_f32_ubyte2_e32 v87, v43
	v_cvt_f32_ubyte3_e32 v88, v43
	v_fmac_f32_e32 v14, v85, v57
	v_fmac_f32_e32 v15, v86, v57
	v_fmac_f32_e32 v16, v87, v57
	v_fmac_f32_e32 v17, v88, v57
	v_add_f32_e32 v18, v18, v57
	global_load_dwordx4 v[40:43], v103, s[8:9] offset:272
	s_waitcnt vmcnt(7)
	v_cvt_f32_ubyte0_e32 v85, v44
	v_cvt_f32_ubyte1_e32 v86, v44
	v_cvt_f32_ubyte2_e32 v87, v44
	v_cvt_f32_ubyte3_e32 v88, v44
	v_fmac_f32_e32 v2, v85, v58
	v_fmac_f32_e32 v3, v86, v58
	v_fmac_f32_e32 v4, v87, v58
	v_fmac_f32_e32 v5, v88, v58
	v_cvt_f32_ubyte0_e32 v85, v45
	v_cvt_f32_ubyte1_e32 v86, v45
	v_cvt_f32_ubyte2_e32 v87, v45
	v_cvt_f32_ubyte3_e32 v88, v45
	v_fmac_f32_e32 v6, v85, v58
	v_fmac_f32_e32 v7, v86, v58
	v_fmac_f32_e32 v8, v87, v58
	v_fmac_f32_e32 v9, v88, v58
	v_cvt_f32_ubyte0_e32 v85, v46
	v_cvt_f32_ubyte1_e32 v86, v46
	v_cvt_f32_ubyte2_e32 v87, v46
	v_cvt_f32_ubyte3_e32 v88, v46
	v_fmac_f32_e32 v10, v85, v58
	v_fmac_f32_e32 v11, v86, v58
	v_fmac_f32_e32 v12, v87, v58
	v_fmac_f32_e32 v13, v88, v58
	v_cvt_f32_ubyte0_e32 v85, v47
	v_cvt_f32_ubyte1_e32 v86, v47
	v_cvt_f32_ubyte2_e32 v87, v47
	v_cvt_f32_ubyte3_e32 v88, v47
	v_fmac_f32_e32 v14, v85, v58
	v_fmac_f32_e32 v15, v86, v58
	v_fmac_f32_e32 v16, v87, v58
	v_fmac_f32_e32 v17, v88, v58
	v_add_f32_e32 v18, v18, v58
	global_load_dwordx4 v[44:47], v103, s[8:9] offset:384
	s_waitcnt vmcnt(7)
	v_cvt_f32_ubyte0_e32 v85, v48
	v_cvt_f32_ubyte1_e32 v86, v48
	v_cvt_f32_ubyte2_e32 v87, v48
	v_cvt_f32_ubyte3_e32 v88, v48
	v_fmac_f32_e32 v2, v85, v59
	v_fmac_f32_e32 v3, v86, v59
	v_fmac_f32_e32 v4, v87, v59
	v_fmac_f32_e32 v5, v88, v59
	v_cvt_f32_ubyte0_e32 v85, v49
	v_cvt_f32_ubyte1_e32 v86, v49
	v_cvt_f32_ubyte2_e32 v87, v49
	v_cvt_f32_ubyte3_e32 v88, v49
	v_fmac_f32_e32 v6, v85, v59
	v_fmac_f32_e32 v7, v86, v59
	v_fmac_f32_e32 v8, v87, v59
	v_fmac_f32_e32 v9, v88, v59
	v_cvt_f32_ubyte0_e32 v85, v50
	v_cvt_f32_ubyte1_e32 v86, v50
	v_cvt_f32_ubyte2_e32 v87, v50
	v_cvt_f32_ubyte3_e32 v88, v50
	v_fmac_f32_e32 v10, v85, v59
	v_fmac_f32_e32 v11, v86, v59
	v_fmac_f32_e32 v12, v87, v59
	v_fmac_f32_e32 v13, v88, v59
	v_cvt_f32_ubyte0_e32 v85, v51
	v_cvt_f32_ubyte1_e32 v86, v51
	v_cvt_f32_ubyte2_e32 v87, v51
	v_cvt_f32_ubyte3_e32 v88, v51
	v_fmac_f32_e32 v14, v85, v59
	v_fmac_f32_e32 v15, v86, v59
	v_fmac_f32_e32 v16, v87, v59
	v_fmac_f32_e32 v17, v88, v59
	v_add_f32_e32 v18, v18, v59
	global_load_dwordx4 v[48:51], v103, s[8:9] offset:400
	s_waitcnt vmcnt(7)
	v_cvt_f32_ubyte0_e32 v85, v20
	v_cvt_f32_ubyte1_e32 v86, v20
	v_cvt_f32_ubyte2_e32 v87, v20
	v_cvt_f32_ubyte3_e32 v88, v20
	v_fmac_f32_e32 v2, v85, v52
	v_fmac_f32_e32 v3, v86, v52
	v_fmac_f32_e32 v4, v87, v52
	v_fmac_f32_e32 v5, v88, v52
	v_cvt_f32_ubyte0_e32 v85, v21
	v_cvt_f32_ubyte1_e32 v86, v21
	v_cvt_f32_ubyte2_e32 v87, v21
	v_cvt_f32_ubyte3_e32 v88, v21
	v_fmac_f32_e32 v6, v85, v52
	v_fmac_f32_e32 v7, v86, v52
	v_fmac_f32_e32 v8, v87, v52
	v_fmac_f32_e32 v9, v88, v52
	v_cvt_f32_ubyte0_e32 v85, v22
	v_cvt_f32_ubyte1_e32 v86, v22
	v_cvt_f32_ubyte2_e32 v87, v22
	v_cvt_f32_ubyte3_e32 v88, v22
	v_fmac_f32_e32 v10, v85, v52
	v_fmac_f32_e32 v11, v86, v52
	v_fmac_f32_e32 v12, v87, v52
	v_fmac_f32_e32 v13, v88, v52
	v_cvt_f32_ubyte0_e32 v85, v23
	v_cvt_f32_ubyte1_e32 v86, v23
	v_cvt_f32_ubyte2_e32 v87, v23
	v_cvt_f32_ubyte3_e32 v88, v23
	v_fmac_f32_e32 v14, v85, v52
	v_fmac_f32_e32 v15, v86, v52
	v_fmac_f32_e32 v16, v87, v52
	v_fmac_f32_e32 v17, v88, v52
	v_add_f32_e32 v18, v18, v52
	global_load_dwordx4 v[20:23], v103, s[8:9] offset:0
	s_waitcnt vmcnt(7)
	v_cvt_f32_ubyte0_e32 v85, v24
	v_cvt_f32_ubyte1_e32 v86, v24
	v_cvt_f32_ubyte2_e32 v87, v24
	v_cvt_f32_ubyte3_e32 v88, v24
	v_fmac_f32_e32 v2, v85, v53
	v_fmac_f32_e32 v3, v86, v53
	v_fmac_f32_e32 v4, v87, v53
	v_fmac_f32_e32 v5, v88, v53
	v_cvt_f32_ubyte0_e32 v85, v25
	v_cvt_f32_ubyte1_e32 v86, v25
	v_cvt_f32_ubyte2_e32 v87, v25
	v_cvt_f32_ubyte3_e32 v88, v25
	v_fmac_f32_e32 v6, v85, v53
	v_fmac_f32_e32 v7, v86, v53
	v_fmac_f32_e32 v8, v87, v53
	v_fmac_f32_e32 v9, v88, v53
	v_cvt_f32_ubyte0_e32 v85, v26
	v_cvt_f32_ubyte1_e32 v86, v26
	v_cvt_f32_ubyte2_e32 v87, v26
	v_cvt_f32_ubyte3_e32 v88, v26
	v_fmac_f32_e32 v10, v85, v53
	v_fmac_f32_e32 v11, v86, v53
	v_fmac_f32_e32 v12, v87, v53
	v_fmac_f32_e32 v13, v88, v53
	v_cvt_f32_ubyte0_e32 v85, v27
	v_cvt_f32_ubyte1_e32 v86, v27
	v_cvt_f32_ubyte2_e32 v87, v27
	v_cvt_f32_ubyte3_e32 v88, v27
	v_fmac_f32_e32 v14, v85, v53
	v_fmac_f32_e32 v15, v86, v53
	v_fmac_f32_e32 v16, v87, v53
	v_fmac_f32_e32 v17, v88, v53
	v_add_f32_e32 v18, v18, v53
	global_load_dwordx4 v[24:27], v103, s[8:9] offset:16
	s_waitcnt vmcnt(7)
	v_cvt_f32_ubyte0_e32 v85, v28
	v_cvt_f32_ubyte1_e32 v86, v28
	v_cvt_f32_ubyte2_e32 v87, v28
	v_cvt_f32_ubyte3_e32 v88, v28
	v_fmac_f32_e32 v2, v85, v54
	v_fmac_f32_e32 v3, v86, v54
	v_fmac_f32_e32 v4, v87, v54
	v_fmac_f32_e32 v5, v88, v54
	v_cvt_f32_ubyte0_e32 v85, v29
	v_cvt_f32_ubyte1_e32 v86, v29
	v_cvt_f32_ubyte2_e32 v87, v29
	v_cvt_f32_ubyte3_e32 v88, v29
	v_fmac_f32_e32 v6, v85, v54
	v_fmac_f32_e32 v7, v86, v54
	v_fmac_f32_e32 v8, v87, v54
	v_fmac_f32_e32 v9, v88, v54
	v_cvt_f32_ubyte0_e32 v85, v30
	v_cvt_f32_ubyte1_e32 v86, v30
	v_cvt_f32_ubyte2_e32 v87, v30
	v_cvt_f32_ubyte3_e32 v88, v30
	v_fmac_f32_e32 v10, v85, v54
	v_fmac_f32_e32 v11, v86, v54
	v_fmac_f32_e32 v12, v87, v54
	v_fmac_f32_e32 v13, v88, v54
	v_cvt_f32_ubyte0_e32 v85, v31
	v_cvt_f32_ubyte1_e32 v86, v31
	v_cvt_f32_ubyte2_e32 v87, v31
	v_cvt_f32_ubyte3_e32 v88, v31
	v_fmac_f32_e32 v14, v85, v54
	v_fmac_f32_e32 v15, v86, v54
	v_fmac_f32_e32 v16, v87, v54
	v_fmac_f32_e32 v17, v88, v54
	v_add_f32_e32 v18, v18, v54
	global_load_dwordx4 v[28:31], v103, s[8:9] offset:128
	s_waitcnt vmcnt(7)
	v_cvt_f32_ubyte0_e32 v85, v32
	v_cvt_f32_ubyte1_e32 v86, v32
	v_cvt_f32_ubyte2_e32 v87, v32
	v_cvt_f32_ubyte3_e32 v88, v32
	v_fmac_f32_e32 v2, v85, v55
	v_fmac_f32_e32 v3, v86, v55
	v_fmac_f32_e32 v4, v87, v55
	v_fmac_f32_e32 v5, v88, v55
	v_cvt_f32_ubyte0_e32 v85, v33
	v_cvt_f32_ubyte1_e32 v86, v33
	v_cvt_f32_ubyte2_e32 v87, v33
	v_cvt_f32_ubyte3_e32 v88, v33
	v_fmac_f32_e32 v6, v85, v55
	v_fmac_f32_e32 v7, v86, v55
	v_fmac_f32_e32 v8, v87, v55
	v_fmac_f32_e32 v9, v88, v55
	v_cvt_f32_ubyte0_e32 v85, v34
	v_cvt_f32_ubyte1_e32 v86, v34
	v_cvt_f32_ubyte2_e32 v87, v34
	v_cvt_f32_ubyte3_e32 v88, v34
	v_fmac_f32_e32 v10, v85, v55
	v_fmac_f32_e32 v11, v86, v55
	v_fmac_f32_e32 v12, v87, v55
	v_fmac_f32_e32 v13, v88, v55
	v_cvt_f32_ubyte0_e32 v85, v35
	v_cvt_f32_ubyte1_e32 v86, v35
	v_cvt_f32_ubyte2_e32 v87, v35
	v_cvt_f32_ubyte3_e32 v88, v35
	v_fmac_f32_e32 v14, v85, v55
	v_fmac_f32_e32 v15, v86, v55
	v_fmac_f32_e32 v16, v87, v55
	v_fmac_f32_e32 v17, v88, v55
	v_add_f32_e32 v18, v18, v55
	global_load_dwordx4 v[32:35], v103, s[8:9] offset:144
	s_branch .Lg1_rare_check

.Lg1_rare_loop:
	v_mov_b32_e32 v84, 0xc350
	v_cmp_lt_i32_e32 vcc, s42, v78
	v_add_u32_e32 v83, s42, v77
	v_lshlrev_b32_e32 v83, 2, v83
	s_and_saveexec_b64 s[44:45], vcc
	global_load_dword v84, v83, s[20:21]
	s_or_b64 exec, exec, s[44:45]
	s_waitcnt vmcnt(0)
	v_lshlrev_b32_e32 v83, 1, v84
	global_load_ushort v19, v83, s[14:15]
	v_lshl_or_b32 v83, v84, 7, v89
	global_load_dwordx4 v[94:97], v83, s[12:13]
	s_waitcnt vmcnt(0)
	v_cvt_f32_f16_e32 v19, v19
	v_cvt_f32_ubyte0_e32 v85, v94
	v_cvt_f32_ubyte1_e32 v86, v94
	v_cvt_f32_ubyte2_e32 v87, v94
	v_cvt_f32_ubyte3_e32 v88, v94
	v_fmac_f32_e32 v2, v85, v19
	v_fmac_f32_e32 v3, v86, v19
	v_fmac_f32_e32 v4, v87, v19
	v_fmac_f32_e32 v5, v88, v19
	v_cvt_f32_ubyte0_e32 v85, v95
	v_cvt_f32_ubyte1_e32 v86, v95
	v_cvt_f32_ubyte2_e32 v87, v95
	v_cvt_f32_ubyte3_e32 v88, v95
	v_fmac_f32_e32 v6, v85, v19
	v_fmac_f32_e32 v7, v86, v19
	v_fmac_f32_e32 v8, v87, v19
	v_fmac_f32_e32 v9, v88, v19
	v_cvt_f32_ubyte0_e32 v85, v96
	v_cvt_f32_ubyte1_e32 v86, v96
	v_cvt_f32_ubyte2_e32 v87, v96
	v_cvt_f32_ubyte3_e32 v88, v96
	v_fmac_f32_e32 v10, v85, v19
	v_fmac_f32_e32 v11, v86, v19
	v_fmac_f32_e32 v12, v87, v19
	v_fmac_f32_e32 v13, v88, v19
	v_cvt_f32_ubyte0_e32 v85, v97
	v_cvt_f32_ubyte1_e32 v86, v97
	v_cvt_f32_ubyte2_e32 v87, v97
	v_cvt_f32_ubyte3_e32 v88, v97
	v_fmac_f32_e32 v14, v85, v19
	v_fmac_f32_e32 v15, v86, v19
	v_fmac_f32_e32 v16, v87, v19
	v_fmac_f32_e32 v17, v88, v19
	v_add_f32_e32 v18, v18, v19
	s_add_i32 s42, s42, 1
	s_cmp_lt_i32 s42, s41
	s_cbranch_scc1 .Lg1_rare_loop
.Lg1_final:
	v_max_i32_e32 v94, 1, v78
	v_cvt_f32_u32_e32 v94, v94
	v_div_scale_f32 v96, s[62:63], v94, v94, 1.0
	v_rcp_f32_e32 v97, v96
	v_div_scale_f32 v98, vcc, 1.0, v94, 1.0
	v_fma_f32 v99, -v96, v97, 1.0
	v_fmac_f32_e32 v97, v99, v97
	v_mul_f32_e32 v99, v98, v97
	v_fma_f32 v95, -v96, v99, v98
	v_fmac_f32_e32 v99, v95, v97
	v_fma_f32 v96, -v96, v99, v98
	v_div_fmas_f32 v96, v96, v97, v99
	v_div_fixup_f32 v95, v96, v94, 1.0
	v_mul_f32_e32 v18, 0x43000000, v18
	v_sub_f32_e32 v2, v2, v18
	v_sub_f32_e32 v3, v3, v18
	v_sub_f32_e32 v4, v4, v18
	v_sub_f32_e32 v5, v5, v18
	v_sub_f32_e32 v6, v6, v18
	v_sub_f32_e32 v7, v7, v18
	v_sub_f32_e32 v8, v8, v18
	v_sub_f32_e32 v9, v9, v18
	v_sub_f32_e32 v10, v10, v18
	v_sub_f32_e32 v11, v11, v18
	v_sub_f32_e32 v12, v12, v18
	v_sub_f32_e32 v13, v13, v18
	v_sub_f32_e32 v14, v14, v18
	v_sub_f32_e32 v15, v15, v18
	v_sub_f32_e32 v16, v16, v18
	v_sub_f32_e32 v17, v17, v18
	v_mul_f32_e32 v2, v95, v2
	v_mul_f32_e32 v3, v95, v3
	v_mul_f32_e32 v4, v95, v4
	v_mul_f32_e32 v5, v95, v5
	v_mul_f32_e32 v6, v95, v6
	v_mul_f32_e32 v7, v95, v7
	v_mul_f32_e32 v8, v95, v8
	v_mul_f32_e32 v9, v95, v9
	v_mul_f32_e32 v10, v95, v10
	v_mul_f32_e32 v11, v95, v11
	v_mul_f32_e32 v12, v95, v12
	v_mul_f32_e32 v13, v95, v13
	v_mul_f32_e32 v14, v95, v14
	v_mul_f32_e32 v15, v95, v15
	v_mul_f32_e32 v16, v95, v16
	v_mul_f32_e32 v17, v95, v17
	v_cvt_pk_f16_f32 v52, v2, v3
	v_cvt_pk_f16_f32 v53, v4, v5
	v_cvt_pk_f16_f32 v54, v6, v7
	v_cvt_pk_f16_f32 v55, v8, v9
	v_cvt_pk_f16_f32 v56, v10, v11
	v_cvt_pk_f16_f32 v57, v12, v13
	v_cvt_pk_f16_f32 v58, v14, v15
	v_cvt_pk_f16_f32 v59, v16, v17
	ds_write_b128 v93, v[52:55]
	ds_write_b128 v93, v[56:59] offset:16
	s_add_u32 s39, s39, 1
	s_cmp_lt_u32 s39, 2
	s_cbranch_scc1 .Lg1_set_top
	s_waitcnt vmcnt(0)
	v_cvt_pk_f16_f32 v112, v20, v21
	v_cvt_pk_f16_f32 v113, v22, v23
	v_cvt_pk_f16_f32 v114, v24, v25
	v_cvt_pk_f16_f32 v115, v26, v27
	v_cvt_pk_f16_f32 v116, v28, v29
	v_cvt_pk_f16_f32 v117, v30, v31
	v_cvt_pk_f16_f32 v118, v32, v33
	v_cvt_pk_f16_f32 v119, v34, v35
	v_cvt_pk_f16_f32 v120, v36, v37
	v_cvt_pk_f16_f32 v121, v38, v39
	v_cvt_pk_f16_f32 v122, v40, v41
	v_cvt_pk_f16_f32 v123, v42, v43
	v_cvt_pk_f16_f32 v124, v44, v45
	v_cvt_pk_f16_f32 v125, v46, v47
	v_cvt_pk_f16_f32 v126, v48, v49
	v_cvt_pk_f16_f32 v127, v50, v51
	v_lshlrev_b32_e32 v107, 9, v105
	v_xor_b32_e32 v108, v106, v105
	v_lshlrev_b32_e32 v108, 4, v108
	v_mul_u32_u24_e32 v109, 0x110, v105
	v_lshl_add_u32 v109, v106, 4, v109
	v_add_u32_e32 v109, s48, v109
	v_lshlrev_b32_e32 v110, 4, v106
	v_add_u32_e32 v110, 0x10000, v110
	ds_read_b128 v[4:7], v110 offset:0
	ds_read_b128 v[8:11], v110 offset:64
	ds_read_b128 v[12:15], v110 offset:128
	ds_read_b128 v[16:19], v110 offset:192
	ds_read_b128 v[20:23], v110 offset:256
	ds_read_b128 v[24:27], v110 offset:320
	ds_read_b128 v[28:31], v110 offset:384
	ds_read_b128 v[32:35], v110 offset:448
	v_xor_b32_e32 v111, 0, v108
	v_add_u32_e32 v111, v111, v107
	ds_read_b128 v[100:103], v109
	ds_read_b128 v[36:39], v111 offset:0
	ds_read_b128 v[40:43], v111 offset:8192
	ds_read_b128 v[44:47], v111 offset:16384
	ds_read_b128 v[48:51], v111 offset:24576
	ds_read_b128 v[52:55], v111 offset:32768
	ds_read_b128 v[56:59], v111 offset:40960
	s_waitcnt lgkmcnt(7)
	ds_read_b128 v[60:63], v111 offset:49152
	ds_read_b128 v[64:67], v111 offset:57344
	s_waitcnt lgkmcnt(0)
	v_xor_b32_e32 v111, 64, v108
	v_add_u32_e32 v111, v111, v107
	ds_read_b128 v[0:3], v109 offset:64
	ds_read_b128 v[68:71], v111 offset:0
	ds_read_b128 v[72:75], v111 offset:8192
	ds_read_b128 v[76:79], v111 offset:16384
	ds_read_b128 v[80:83], v111 offset:24576
	ds_read_b128 v[84:87], v111 offset:32768
	ds_read_b128 v[88:91], v111 offset:40960
	ds_read_b128 v[92:95], v111 offset:49152
	ds_read_b128 v[96:99], v111 offset:57344
	v_mfma_f32_16x16x32_f16 v[4:7], v[36:39], v[100:103], v[4:7]
	v_mfma_f32_16x16x32_f16 v[8:11], v[40:43], v[100:103], v[8:11]
	v_mfma_f32_16x16x32_f16 v[12:15], v[44:47], v[100:103], v[12:15]
	v_mfma_f32_16x16x32_f16 v[16:19], v[48:51], v[100:103], v[16:19]
	v_mfma_f32_16x16x32_f16 v[20:23], v[52:55], v[100:103], v[20:23]
	v_mfma_f32_16x16x32_f16 v[24:27], v[56:59], v[100:103], v[24:27]
	v_mfma_f32_16x16x32_f16 v[28:31], v[60:63], v[100:103], v[28:31]
	v_mfma_f32_16x16x32_f16 v[32:35], v[64:67], v[100:103], v[32:35]
	s_waitcnt lgkmcnt(0)
	v_xor_b32_e32 v111, 128, v108
	v_add_u32_e32 v111, v111, v107
	ds_read_b128 v[100:103], v109 offset:128
	ds_read_b128 v[36:39], v111 offset:0
	ds_read_b128 v[40:43], v111 offset:8192
	ds_read_b128 v[44:47], v111 offset:16384
	ds_read_b128 v[48:51], v111 offset:24576
	ds_read_b128 v[52:55], v111 offset:32768
	ds_read_b128 v[56:59], v111 offset:40960
	ds_read_b128 v[60:63], v111 offset:49152
	ds_read_b128 v[64:67], v111 offset:57344
	v_mfma_f32_16x16x32_f16 v[4:7], v[68:71], v[0:3], v[4:7]
	v_mfma_f32_16x16x32_f16 v[8:11], v[72:75], v[0:3], v[8:11]
	v_mfma_f32_16x16x32_f16 v[12:15], v[76:79], v[0:3], v[12:15]
	v_mfma_f32_16x16x32_f16 v[16:19], v[80:83], v[0:3], v[16:19]
	v_mfma_f32_16x16x32_f16 v[20:23], v[84:87], v[0:3], v[20:23]
	v_mfma_f32_16x16x32_f16 v[24:27], v[88:91], v[0:3], v[24:27]
	v_mfma_f32_16x16x32_f16 v[28:31], v[92:95], v[0:3], v[28:31]
	v_mfma_f32_16x16x32_f16 v[32:35], v[96:99], v[0:3], v[32:35]
	s_waitcnt lgkmcnt(0)
	v_xor_b32_e32 v111, 192, v108
	v_add_u32_e32 v111, v111, v107
	ds_read_b128 v[0:3], v109 offset:192
	ds_read_b128 v[68:71], v111 offset:0
	ds_read_b128 v[72:75], v111 offset:8192
	ds_read_b128 v[76:79], v111 offset:16384
	ds_read_b128 v[80:83], v111 offset:24576
	ds_read_b128 v[84:87], v111 offset:32768
	ds_read_b128 v[88:91], v111 offset:40960
	ds_read_b128 v[92:95], v111 offset:49152
	ds_read_b128 v[96:99], v111 offset:57344
	v_mfma_f32_16x16x32_f16 v[4:7], v[36:39], v[100:103], v[4:7]
	v_mfma_f32_16x16x32_f16 v[8:11], v[40:43], v[100:103], v[8:11]
	v_mfma_f32_16x16x32_f16 v[12:15], v[44:47], v[100:103], v[12:15]
	v_mfma_f32_16x16x32_f16 v[16:19], v[48:51], v[100:103], v[16:19]
	v_mfma_f32_16x16x32_f16 v[20:23], v[52:55], v[100:103], v[20:23]
	v_mfma_f32_16x16x32_f16 v[24:27], v[56:59], v[100:103], v[24:27]
	v_mfma_f32_16x16x32_f16 v[28:31], v[60:63], v[100:103], v[28:31]
	v_mfma_f32_16x16x32_f16 v[32:35], v[64:67], v[100:103], v[32:35]
	s_waitcnt lgkmcnt(0)
	v_xor_b32_e32 v111, 256, v108
	v_add_u32_e32 v111, v111, v107
	ds_read_b128 v[36:39], v111 offset:0
	ds_read_b128 v[40:43], v111 offset:8192
	ds_read_b128 v[44:47], v111 offset:16384
	ds_read_b128 v[48:51], v111 offset:24576
	ds_read_b128 v[52:55], v111 offset:32768
	ds_read_b128 v[56:59], v111 offset:40960
	ds_read_b128 v[60:63], v111 offset:49152
	ds_read_b128 v[64:67], v111 offset:57344
	v_mfma_f32_16x16x32_f16 v[4:7], v[68:71], v[0:3], v[4:7]
	v_mfma_f32_16x16x32_f16 v[8:11], v[72:75], v[0:3], v[8:11]
	v_mfma_f32_16x16x32_f16 v[12:15], v[76:79], v[0:3], v[12:15]
	v_mfma_f32_16x16x32_f16 v[16:19], v[80:83], v[0:3], v[16:19]
	v_mfma_f32_16x16x32_f16 v[20:23], v[84:87], v[0:3], v[20:23]
	v_mfma_f32_16x16x32_f16 v[24:27], v[88:91], v[0:3], v[24:27]
	v_mfma_f32_16x16x32_f16 v[28:31], v[92:95], v[0:3], v[28:31]
	v_mfma_f32_16x16x32_f16 v[32:35], v[96:99], v[0:3], v[32:35]
	s_waitcnt lgkmcnt(0)
	s_waitcnt vmcnt(0)
	v_xor_b32_e32 v111, 320, v108
	v_add_u32_e32 v111, v111, v107
	ds_read_b128 v[68:71], v111 offset:0
	ds_read_b128 v[72:75], v111 offset:8192
	ds_read_b128 v[76:79], v111 offset:16384
	ds_read_b128 v[80:83], v111 offset:24576
	ds_read_b128 v[84:87], v111 offset:32768
	ds_read_b128 v[88:91], v111 offset:40960
	ds_read_b128 v[92:95], v111 offset:49152
	ds_read_b128 v[96:99], v111 offset:57344
	v_mfma_f32_16x16x32_f16 v[4:7], v[36:39], v[112:115], v[4:7]
	v_mfma_f32_16x16x32_f16 v[8:11], v[40:43], v[112:115], v[8:11]
	v_mfma_f32_16x16x32_f16 v[12:15], v[44:47], v[112:115], v[12:15]
	v_mfma_f32_16x16x32_f16 v[16:19], v[48:51], v[112:115], v[16:19]
	v_mfma_f32_16x16x32_f16 v[20:23], v[52:55], v[112:115], v[20:23]
	v_mfma_f32_16x16x32_f16 v[24:27], v[56:59], v[112:115], v[24:27]
	v_mfma_f32_16x16x32_f16 v[28:31], v[60:63], v[112:115], v[28:31]
	v_mfma_f32_16x16x32_f16 v[32:35], v[64:67], v[112:115], v[32:35]
	s_waitcnt lgkmcnt(0)
	v_xor_b32_e32 v111, 384, v108
	v_add_u32_e32 v111, v111, v107
	ds_read_b128 v[36:39], v111 offset:0
	ds_read_b128 v[40:43], v111 offset:8192
	ds_read_b128 v[44:47], v111 offset:16384
	ds_read_b128 v[48:51], v111 offset:24576
	ds_read_b128 v[52:55], v111 offset:32768
	ds_read_b128 v[56:59], v111 offset:40960
	ds_read_b128 v[60:63], v111 offset:49152
	ds_read_b128 v[64:67], v111 offset:57344
	v_mfma_f32_16x16x32_f16 v[4:7], v[68:71], v[116:119], v[4:7]
	v_mfma_f32_16x16x32_f16 v[8:11], v[72:75], v[116:119], v[8:11]
	v_mfma_f32_16x16x32_f16 v[12:15], v[76:79], v[116:119], v[12:15]
	v_mfma_f32_16x16x32_f16 v[16:19], v[80:83], v[116:119], v[16:19]
	v_mfma_f32_16x16x32_f16 v[20:23], v[84:87], v[116:119], v[20:23]
	v_mfma_f32_16x16x32_f16 v[24:27], v[88:91], v[116:119], v[24:27]
	v_mfma_f32_16x16x32_f16 v[28:31], v[92:95], v[116:119], v[28:31]
	v_mfma_f32_16x16x32_f16 v[32:35], v[96:99], v[116:119], v[32:35]
	s_waitcnt lgkmcnt(0)
	v_xor_b32_e32 v111, 448, v108
	v_add_u32_e32 v111, v111, v107
	ds_read_b128 v[68:71], v111 offset:0
	ds_read_b128 v[72:75], v111 offset:8192
	ds_read_b128 v[76:79], v111 offset:16384
	ds_read_b128 v[80:83], v111 offset:24576
	ds_read_b128 v[84:87], v111 offset:32768
	ds_read_b128 v[88:91], v111 offset:40960
	ds_read_b128 v[92:95], v111 offset:49152
	ds_read_b128 v[96:99], v111 offset:57344
	v_mfma_f32_16x16x32_f16 v[4:7], v[36:39], v[120:123], v[4:7]
	v_mfma_f32_16x16x32_f16 v[8:11], v[40:43], v[120:123], v[8:11]
	v_mfma_f32_16x16x32_f16 v[12:15], v[44:47], v[120:123], v[12:15]
	v_mfma_f32_16x16x32_f16 v[16:19], v[48:51], v[120:123], v[16:19]
	v_mfma_f32_16x16x32_f16 v[20:23], v[52:55], v[120:123], v[20:23]
	v_mfma_f32_16x16x32_f16 v[24:27], v[56:59], v[120:123], v[24:27]
	v_mfma_f32_16x16x32_f16 v[28:31], v[60:63], v[120:123], v[28:31]
	v_mfma_f32_16x16x32_f16 v[32:35], v[64:67], v[120:123], v[32:35]
	s_waitcnt lgkmcnt(0)
	v_mfma_f32_16x16x32_f16 v[4:7], v[68:71], v[124:127], v[4:7]
	v_mfma_f32_16x16x32_f16 v[8:11], v[72:75], v[124:127], v[8:11]
	v_mfma_f32_16x16x32_f16 v[12:15], v[76:79], v[124:127], v[12:15]
	v_mfma_f32_16x16x32_f16 v[16:19], v[80:83], v[124:127], v[16:19]
	v_mfma_f32_16x16x32_f16 v[20:23], v[84:87], v[124:127], v[20:23]
	v_mfma_f32_16x16x32_f16 v[24:27], v[88:91], v[124:127], v[24:27]
	v_mfma_f32_16x16x32_f16 v[28:31], v[92:95], v[124:127], v[28:31]
	v_mfma_f32_16x16x32_f16 v[32:35], v[96:99], v[124:127], v[32:35]
	s_nop 7
	s_nop 3
	v_max_f32_e32 v4, 0, v4
	v_max_f32_e32 v5, 0, v5
	v_max_f32_e32 v6, 0, v6
	v_max_f32_e32 v7, 0, v7
	v_max_f32_e32 v8, 0, v8
	v_max_f32_e32 v9, 0, v9
	v_max_f32_e32 v10, 0, v10
	v_max_f32_e32 v11, 0, v11
	v_max_f32_e32 v12, 0, v12
	v_max_f32_e32 v13, 0, v13
	v_max_f32_e32 v14, 0, v14
	v_max_f32_e32 v15, 0, v15
	v_max_f32_e32 v16, 0, v16
	v_max_f32_e32 v17, 0, v17
	v_max_f32_e32 v18, 0, v18
	v_max_f32_e32 v19, 0, v19
	v_max_f32_e32 v20, 0, v20
	v_max_f32_e32 v21, 0, v21
	v_max_f32_e32 v22, 0, v22
	v_max_f32_e32 v23, 0, v23
	v_max_f32_e32 v24, 0, v24
	v_max_f32_e32 v25, 0, v25
	v_max_f32_e32 v26, 0, v26
	v_max_f32_e32 v27, 0, v27
	v_max_f32_e32 v28, 0, v28
	v_max_f32_e32 v29, 0, v29
	v_max_f32_e32 v30, 0, v30
	v_max_f32_e32 v31, 0, v31
	v_max_f32_e32 v32, 0, v32
	v_max_f32_e32 v33, 0, v33
	v_max_f32_e32 v34, 0, v34
	v_max_f32_e32 v35, 0, v35
	v_max3_f32 v37, v4, v5, v6
	v_max3_f32 v37, v37, v7, v8
	v_max3_f32 v37, v37, v9, v10
	v_max3_f32 v37, v37, v11, v12
	v_max3_f32 v37, v37, v13, v14
	v_max3_f32 v37, v37, v15, v16
	v_max3_f32 v37, v37, v17, v18
	v_max3_f32 v37, v37, v19, v20
	v_max3_f32 v37, v37, v21, v22
	v_max3_f32 v37, v37, v23, v24
	v_max3_f32 v37, v37, v25, v26
	v_max3_f32 v37, v37, v27, v28
	v_max3_f32 v37, v37, v29, v30
	v_max3_f32 v37, v37, v31, v32
	v_max3_f32 v37, v37, v33, v34
	v_max_f32_e32 v37, v37, v35
	v_lshl_or_b32 v36, v106, 4, v105
	v_xor_b32_e32 v38, 16, v36
	v_lshlrev_b32_e32 v38, 2, v38
	ds_bpermute_b32 v39, v38, v37
	s_waitcnt lgkmcnt(0)
	v_max_f32_e32 v37, v37, v39
	v_xor_b32_e32 v38, 32, v36
	v_lshlrev_b32_e32 v38, 2, v38
	ds_bpermute_b32 v39, v38, v37
	s_waitcnt lgkmcnt(0)
	v_max_f32_e32 v37, v37, v39
	s_mov_b32 s58, 0x437f0000
	v_div_scale_f32 v41, s[62:63], v37, v37, s58
	v_rcp_f32_e32 v42, v41
	v_div_scale_f32 v43, vcc, s58, v37, s58
	v_fma_f32 v44, -v41, v42, 1.0
	v_fmac_f32_e32 v42, v44, v42
	v_mul_f32_e32 v44, v43, v42
	v_fma_f32 v40, -v41, v44, v43
	v_fmac_f32_e32 v44, v40, v42
	v_fma_f32 v41, -v41, v44, v43
	v_div_fmas_f32 v41, v41, v42, v44
	v_div_fixup_f32 v40, v41, v37, s58
	v_cmp_lt_f32_e32 vcc, 0, v37
	s_nop 1
	v_cndmask_b32_e32 v40, 0, v40, vcc
	v_mul_u32_u24_e32 v45, 0x110, v105
	v_lshl_add_u32 v45, v106, 3, v45
	v_add_u32_e32 v45, s48, v45
	v_mul_u32_u24_e32 v46, 0x110, v106
	v_lshl_add_u32 v46, v105, 4, v46
	v_add_u32_e32 v46, s48, v46
	v_mul_u32_u24_e32 v47, 0x90, v105
	v_lshl_add_u32 v47, v106, 2, v47
	v_add_u32_e32 v47, s48, v47
	v_lshrrev_b32_e32 v50, 3, v36
	v_and_b32_e32 v52, 7, v36
	v_mul_u32_u24_e32 v48, 0x90, v50
	v_lshl_add_u32 v48, v52, 4, v48
	v_add_u32_e32 v48, s48, v48
	v_lshlrev_b32_e32 v50, 2, v50
	v_lshlrev_b32_e32 v52, 4, v52
	v_lshlrev_b32_e32 v49, 2, v106
	v_lshlrev_b32_e32 v51, 4, v105
	ds_bpermute_b32 v53, v49, v104 offset:0
	ds_bpermute_b32 v54, v49, v104 offset:16
	ds_bpermute_b32 v55, v49, v104 offset:32
	ds_bpermute_b32 v56, v49, v104 offset:48
	ds_bpermute_b32 v57, v50, v104 offset:0
	ds_bpermute_b32 v58, v50, v104 offset:32
	s_waitcnt lgkmcnt(0)
	v_cvt_pk_f16_f32 v60, v4, v5
	v_cvt_pk_f16_f32 v61, v6, v7
	ds_write_b64 v45, v[60:61] offset:0
	v_cvt_pk_f16_f32 v60, v8, v9
	v_cvt_pk_f16_f32 v61, v10, v11
	ds_write_b64 v45, v[60:61] offset:32
	v_cvt_pk_f16_f32 v60, v12, v13
	v_cvt_pk_f16_f32 v61, v14, v15
	ds_write_b64 v45, v[60:61] offset:64
	v_cvt_pk_f16_f32 v60, v16, v17
	v_cvt_pk_f16_f32 v61, v18, v19
	ds_write_b64 v45, v[60:61] offset:96
	v_cvt_pk_f16_f32 v60, v20, v21
	v_cvt_pk_f16_f32 v61, v22, v23
	ds_write_b64 v45, v[60:61] offset:128
	v_cvt_pk_f16_f32 v60, v24, v25
	v_cvt_pk_f16_f32 v61, v26, v27
	ds_write_b64 v45, v[60:61] offset:160
	v_cvt_pk_f16_f32 v60, v28, v29
	v_cvt_pk_f16_f32 v61, v30, v31
	ds_write_b64 v45, v[60:61] offset:192
	v_cvt_pk_f16_f32 v60, v32, v33
	v_cvt_pk_f16_f32 v61, v34, v35
	ds_write_b64 v45, v[60:61] offset:224
	ds_read_b128 v[64:67], v46 offset:0
	ds_read_b128 v[68:71], v46 offset:1088
	ds_read_b128 v[72:75], v46 offset:2176
	ds_read_b128 v[76:79], v46 offset:3264
	s_waitcnt lgkmcnt(3)
	v_lshl_or_b32 v53, v53, 8, v51
	global_store_dwordx4 v53, v[64:67], s[26:27] sc1
	s_waitcnt lgkmcnt(2)
	v_lshl_or_b32 v54, v54, 8, v51
	global_store_dwordx4 v54, v[68:71], s[26:27] sc1
	s_waitcnt lgkmcnt(1)
	v_lshl_or_b32 v55, v55, 8, v51
	global_store_dwordx4 v55, v[72:75], s[26:27] sc1
	s_waitcnt lgkmcnt(0)
	v_lshl_or_b32 v56, v56, 8, v51
	global_store_dwordx4 v56, v[76:79], s[26:27] sc1
	v_mul_f32_e32 v80, v40, v4
	v_mul_f32_e32 v81, v40, v5
	v_mul_f32_e32 v82, v40, v6
	v_mul_f32_e32 v83, v40, v7
	v_rndne_f32_e32 v80, v80
	v_rndne_f32_e32 v81, v81
	v_rndne_f32_e32 v82, v82
	v_rndne_f32_e32 v83, v83
	v_cvt_i32_f32_e32 v80, v80
	v_cvt_i32_f32_e32 v81, v81
	v_cvt_i32_f32_e32 v82, v82
	v_cvt_i32_f32_e32 v83, v83
	v_lshl_or_b32 v80, v81, 8, v80
	v_lshl_or_b32 v80, v82, 16, v80
	v_lshl_or_b32 v80, v83, 24, v80
	ds_write_b32 v47, v80 offset:0
	v_mul_f32_e32 v80, v40, v8
	v_mul_f32_e32 v81, v40, v9
	v_mul_f32_e32 v82, v40, v10
	v_mul_f32_e32 v83, v40, v11
	v_rndne_f32_e32 v80, v80
	v_rndne_f32_e32 v81, v81
	v_rndne_f32_e32 v82, v82
	v_rndne_f32_e32 v83, v83
	v_cvt_i32_f32_e32 v80, v80
	v_cvt_i32_f32_e32 v81, v81
	v_cvt_i32_f32_e32 v82, v82
	v_cvt_i32_f32_e32 v83, v83
	v_lshl_or_b32 v80, v81, 8, v80
	v_lshl_or_b32 v80, v82, 16, v80
	v_lshl_or_b32 v80, v83, 24, v80
	ds_write_b32 v47, v80 offset:16
	v_mul_f32_e32 v80, v40, v12
	v_mul_f32_e32 v81, v40, v13
	v_mul_f32_e32 v82, v40, v14
	v_mul_f32_e32 v83, v40, v15
	v_rndne_f32_e32 v80, v80
	v_rndne_f32_e32 v81, v81
	v_rndne_f32_e32 v82, v82
	v_rndne_f32_e32 v83, v83
	v_cvt_i32_f32_e32 v80, v80
	v_cvt_i32_f32_e32 v81, v81
	v_cvt_i32_f32_e32 v82, v82
	v_cvt_i32_f32_e32 v83, v83
	v_lshl_or_b32 v80, v81, 8, v80
	v_lshl_or_b32 v80, v82, 16, v80
	v_lshl_or_b32 v80, v83, 24, v80
	ds_write_b32 v47, v80 offset:32
	v_mul_f32_e32 v80, v40, v16
	v_mul_f32_e32 v81, v40, v17
	v_mul_f32_e32 v82, v40, v18
	v_mul_f32_e32 v83, v40, v19
	v_rndne_f32_e32 v80, v80
	v_rndne_f32_e32 v81, v81
	v_rndne_f32_e32 v82, v82
	v_rndne_f32_e32 v83, v83
	v_cvt_i32_f32_e32 v80, v80
	v_cvt_i32_f32_e32 v81, v81
	v_cvt_i32_f32_e32 v82, v82
	v_cvt_i32_f32_e32 v83, v83
	v_lshl_or_b32 v80, v81, 8, v80
	v_lshl_or_b32 v80, v82, 16, v80
	v_lshl_or_b32 v80, v83, 24, v80
	ds_write_b32 v47, v80 offset:48
	v_mul_f32_e32 v80, v40, v20
	v_mul_f32_e32 v81, v40, v21
	v_mul_f32_e32 v82, v40, v22
	v_mul_f32_e32 v83, v40, v23
	v_rndne_f32_e32 v80, v80
	v_rndne_f32_e32 v81, v81
	v_rndne_f32_e32 v82, v82
	v_rndne_f32_e32 v83, v83
	v_cvt_i32_f32_e32 v80, v80
	v_cvt_i32_f32_e32 v81, v81
	v_cvt_i32_f32_e32 v82, v82
	v_cvt_i32_f32_e32 v83, v83
	v_lshl_or_b32 v80, v81, 8, v80
	v_lshl_or_b32 v80, v82, 16, v80
	v_lshl_or_b32 v80, v83, 24, v80
	ds_write_b32 v47, v80 offset:64
	v_mul_f32_e32 v80, v40, v24
	v_mul_f32_e32 v81, v40, v25
	v_mul_f32_e32 v82, v40, v26
	v_mul_f32_e32 v83, v40, v27
	v_rndne_f32_e32 v80, v80
	v_rndne_f32_e32 v81, v81
	v_rndne_f32_e32 v82, v82
	v_rndne_f32_e32 v83, v83
	v_cvt_i32_f32_e32 v80, v80
	v_cvt_i32_f32_e32 v81, v81
	v_cvt_i32_f32_e32 v82, v82
	v_cvt_i32_f32_e32 v83, v83
	v_lshl_or_b32 v80, v81, 8, v80
	v_lshl_or_b32 v80, v82, 16, v80
	v_lshl_or_b32 v80, v83, 24, v80
	ds_write_b32 v47, v80 offset:80
	v_mul_f32_e32 v80, v40, v28
	v_mul_f32_e32 v81, v40, v29
	v_mul_f32_e32 v82, v40, v30
	v_mul_f32_e32 v83, v40, v31
	v_rndne_f32_e32 v80, v80
	v_rndne_f32_e32 v81, v81
	v_rndne_f32_e32 v82, v82
	v_rndne_f32_e32 v83, v83
	v_cvt_i32_f32_e32 v80, v80
	v_cvt_i32_f32_e32 v81, v81
	v_cvt_i32_f32_e32 v82, v82
	v_cvt_i32_f32_e32 v83, v83
	v_lshl_or_b32 v80, v81, 8, v80
	v_lshl_or_b32 v80, v82, 16, v80
	v_lshl_or_b32 v80, v83, 24, v80
	ds_write_b32 v47, v80 offset:96
	v_mul_f32_e32 v80, v40, v32
	v_mul_f32_e32 v81, v40, v33
	v_mul_f32_e32 v82, v40, v34
	v_mul_f32_e32 v83, v40, v35
	v_rndne_f32_e32 v80, v80
	v_rndne_f32_e32 v81, v81
	v_rndne_f32_e32 v82, v82
	v_rndne_f32_e32 v83, v83
	v_cvt_i32_f32_e32 v80, v80
	v_cvt_i32_f32_e32 v81, v81
	v_cvt_i32_f32_e32 v82, v82
	v_cvt_i32_f32_e32 v83, v83
	v_lshl_or_b32 v80, v81, 8, v80
	v_lshl_or_b32 v80, v82, 16, v80
	v_lshl_or_b32 v80, v83, 24, v80
	ds_write_b32 v47, v80 offset:112
	ds_read_b128 v[84:87], v48 offset:0
	ds_read_b128 v[88:91], v48 offset:1152
	s_waitcnt lgkmcnt(1)
	v_lshl_or_b32 v57, v57, 7, v52
	global_store_dwordx4 v57, v[84:87], s[28:29] sc1
	s_waitcnt lgkmcnt(0)
	v_lshl_or_b32 v58, v58, 7, v52
	global_store_dwordx4 v58, v[88:91], s[28:29] sc1
	v_cmp_eq_u32_e32 vcc, 0, v106
	s_and_saveexec_b64 s[44:45], vcc
	s_mov_b32 s58, 0x3b808081
	v_fma_mixlo_f16 v38, v37, s58, 0
	v_lshlrev_b32_e32 v39, 1, v104
	global_store_short v39, v38, s[30:31]
	s_endpgm
	.p2alignl 8, 3212836864

	.amdhsa_kernel _Z12layer_kernelILb1ELi128EEvPKfPKDF16_PKhS3_PK15HIP_vector_typeIiLj4EEPKtPKiS3_S1_PvPhPDF16_
		.amdhsa_group_segment_fixed_size 0
		.amdhsa_private_segment_fixed_size 0
		.amdhsa_kernarg_size 96
		.amdhsa_user_sgpr_count 2
		.amdhsa_user_sgpr_dispatch_ptr 0
		.amdhsa_user_sgpr_queue_ptr 0
		.amdhsa_user_sgpr_kernarg_segment_ptr 1
		.amdhsa_user_sgpr_dispatch_id 0
		.amdhsa_user_sgpr_kernarg_preload_length 0
		.amdhsa_user_sgpr_kernarg_preload_offset 0
		.amdhsa_user_sgpr_private_segment_size 0
		.amdhsa_uses_dynamic_stack 0
		.amdhsa_enable_private_segment 0
		.amdhsa_system_sgpr_workgroup_id_x 1
		.amdhsa_system_sgpr_workgroup_id_y 0
		.amdhsa_system_sgpr_workgroup_id_z 0
		.amdhsa_system_sgpr_workgroup_info 0
		.amdhsa_system_vgpr_workitem_id 0
		.amdhsa_next_free_vgpr 128
		.amdhsa_next_free_sgpr 64
		.amdhsa_accum_offset 128
		.amdhsa_reserve_vcc 1
		.amdhsa_float_round_mode_32 0
		.amdhsa_float_round_mode_16_64 0
		.amdhsa_float_denorm_mode_32 3
		.amdhsa_float_denorm_mode_16_64 3
		.amdhsa_dx10_clamp 1
		.amdhsa_ieee_mode 1
		.amdhsa_fp16_overflow 0
		.amdhsa_tg_split 0
		.amdhsa_exception_fp_ieee_invalid_op 0
		.amdhsa_exception_fp_denorm_src 0
		.amdhsa_exception_fp_ieee_div_zero 0
		.amdhsa_exception_fp_ieee_overflow 0
		.amdhsa_exception_fp_ieee_underflow 0
		.amdhsa_exception_fp_ieee_inexact 0
		.amdhsa_exception_int_div_zero 0
	.end_amdhsa_kernel

amdhsa.kernels:
  - .agpr_count:     0
    .args:
      - .actual_access:  read_only
        .address_space:  global
        .offset:         0
        .size:           8
        .value_kind:     global_buffer
      - .actual_access:  read_only
        .address_space:  global
        .offset:         8
        .size:           8
        .value_kind:     global_buffer
      - .actual_access:  read_only
        .address_space:  global
        .offset:         16
        .size:           8
        .value_kind:     global_buffer
      - .actual_access:  read_only
        .address_space:  global
        .offset:         24
        .size:           8
        .value_kind:     global_buffer
      - .actual_access:  read_only
        .address_space:  global
        .offset:         32
        .size:           8
        .value_kind:     global_buffer
      - .actual_access:  read_only
        .address_space:  global
        .offset:         40
        .size:           8
        .value_kind:     global_buffer
      - .actual_access:  read_only
        .address_space:  global
        .offset:         48
        .size:           8
        .value_kind:     global_buffer
      - .actual_access:  read_only
        .address_space:  global
        .offset:         56
        .size:           8
        .value_kind:     global_buffer
      - .actual_access:  write_only
        .address_space:  global
        .offset:         64
        .size:           8
        .value_kind:     global_buffer
      - .actual_access:  write_only
        .address_space:  global
        .offset:         72
        .size:           8
        .value_kind:     global_buffer
      - .actual_access:  write_only
        .address_space:  global
        .offset:         80
        .size:           8
        .value_kind:     global_buffer
      - .actual_access:  write_only
        .address_space:  global
        .offset:         88
        .size:           8
        .value_kind:     global_buffer
      - .actual_access:  write_only
        .address_space:  global
        .offset:         96
        .size:           8
        .value_kind:     global_buffer
      - .actual_access:  write_only
        .address_space:  global
        .offset:         104
        .size:           8
        .value_kind:     global_buffer
      - .actual_access:  write_only
        .address_space:  global
        .offset:         112
        .size:           8
        .value_kind:     global_buffer
    .group_segment_fixed_size: 14560
    .kernarg_segment_align: 8
    .kernarg_segment_size: 120
    .language:       OpenCL C
    .language_version:
      - 2
      - 0
    .max_flat_workgroup_size: 1024
    .name:           _Z12sort1_kernelPKfPKiS0_S0_S0_S0_PDF16_S3_S3_S3_PiPjPhS3_S3_
    .private_segment_fixed_size: 0
    .sgpr_count:     26
    .sgpr_spill_count: 0
    .symbol:         _Z12sort1_kernelPKfPKiS0_S0_S0_S0_PDF16_S3_S3_S3_PiPjPhS3_S3_.kd
    .uniform_work_group_size: 1
    .uses_dynamic_stack: false
    .vgpr_count:     31
    .vgpr_spill_count: 0
    .wavefront_size: 64
  - .agpr_count:     0
    .args:
      - .actual_access:  read_only
        .address_space:  global
        .offset:         0
        .size:           8
        .value_kind:     global_buffer
      - .actual_access:  read_only
        .address_space:  global
        .offset:         8
        .size:           8
        .value_kind:     global_buffer
      - .actual_access:  write_only
        .address_space:  global
        .offset:         16
        .size:           8
        .value_kind:     global_buffer
      - .actual_access:  write_only
        .address_space:  global
        .offset:         24
        .size:           8
        .value_kind:     global_buffer
      - .actual_access:  read_only
        .address_space:  global
        .offset:         32
        .size:           8
        .value_kind:     global_buffer
      - .actual_access:  read_only
        .address_space:  global
        .offset:         40
        .size:           8
        .value_kind:     global_buffer
      - .actual_access:  write_only
        .address_space:  global
        .offset:         48
        .size:           8
        .value_kind:     global_buffer
      - .actual_access:  write_only
        .address_space:  global
        .offset:         56
        .size:           8
        .value_kind:     global_buffer
      - .actual_access:  write_only
        .address_space:  global
        .offset:         64
        .size:           8
        .value_kind:     global_buffer
    .group_segment_fixed_size: 21792
    .kernarg_segment_align: 8
    .kernarg_segment_size: 72
    .language:       OpenCL C
    .language_version:
      - 2
      - 0
    .max_flat_workgroup_size: 1024
    .name:           _Z12sort2_kernelPKfPDF16_PhS1_PKiPKjP15HIP_vector_typeIiLj4EEPiPt
    .private_segment_fixed_size: 0
    .sgpr_count:     48
    .sgpr_spill_count: 0
    .symbol:         _Z12sort2_kernelPKfPDF16_PhS1_PKiPKjP15HIP_vector_typeIiLj4EEPiPt.kd
    .uniform_work_group_size: 1
    .uses_dynamic_stack: false
    .vgpr_count:     33
    .vgpr_spill_count: 0
    .wavefront_size: 64
  - .agpr_count:     0
    .args:
      - .actual_access:  read_only
        .address_space:  global
        .offset:         0
        .size:           8
        .value_kind:     global_buffer
      - .actual_access:  read_only
        .address_space:  global
        .offset:         8
        .size:           8
        .value_kind:     global_buffer
      - .actual_access:  read_only
        .address_space:  global
        .offset:         16
        .size:           8
        .value_kind:     global_buffer
      - .actual_access:  read_only
        .address_space:  global
        .offset:         24
        .size:           8
        .value_kind:     global_buffer
      - .actual_access:  read_only
        .address_space:  global
        .offset:         32
        .size:           8
        .value_kind:     global_buffer
      - .actual_access:  read_only
        .address_space:  global
        .offset:         40
        .size:           8
        .value_kind:     global_buffer
      - .actual_access:  read_only
        .address_space:  global
        .offset:         48
        .size:           8
        .value_kind:     global_buffer
      - .actual_access:  read_only
        .address_space:  global
        .offset:         56
        .size:           8
        .value_kind:     global_buffer
      - .actual_access:  read_only
        .address_space:  global
        .offset:         64
        .size:           8
        .value_kind:     global_buffer
      - .actual_access:  write_only
        .address_space:  global
        .offset:         72
        .size:           8
        .value_kind:     global_buffer
      - .actual_access:  write_only
        .address_space:  global
        .offset:         80
        .size:           8
        .value_kind:     global_buffer
      - .actual_access:  write_only
        .address_space:  global
        .offset:         88
        .size:           8
        .value_kind:     global_buffer
    .group_segment_fixed_size: 0
    .kernarg_segment_align: 8
    .kernarg_segment_size: 96
    .language:       OpenCL C
    .language_version:
      - 2
      - 0
    .max_flat_workgroup_size: 1024
    .name:           _Z12layer_kernelILb1ELi128EEvPKfPKDF16_PKhS3_PK15HIP_vector_typeIiLj4EEPKtPKiS3_S1_PvPhPDF16_
    .private_segment_fixed_size: 0
    .sgpr_count:     70
    .sgpr_spill_count: 0
    .symbol:         _Z12layer_kernelILb1ELi128EEvPKfPKDF16_PKhS3_PK15HIP_vector_typeIiLj4EEPKtPKiS3_S1_PvPhPDF16_.kd
    .uniform_work_group_size: 1
    .uses_dynamic_stack: false
    .vgpr_count:     128
    .vgpr_spill_count: 0
    .wavefront_size: 64
  - .agpr_count:     0
    .args:
      - .actual_access:  read_only
        .address_space:  global
        .offset:         0
        .size:           8
        .value_kind:     global_buffer
      - .actual_access:  read_only
        .address_space:  global
        .offset:         8
        .size:           8
        .value_kind:     global_buffer
      - .actual_access:  read_only
        .address_space:  global
        .offset:         16
        .size:           8
        .value_kind:     global_buffer
      - .actual_access:  read_only
        .address_space:  global
        .offset:         24
        .size:           8
        .value_kind:     global_buffer
      - .actual_access:  read_only
        .address_space:  global
        .offset:         32
        .size:           8
        .value_kind:     global_buffer
      - .actual_access:  read_only
        .address_space:  global
        .offset:         40
        .size:           8
        .value_kind:     global_buffer
      - .actual_access:  read_only
        .address_space:  global
        .offset:         48
        .size:           8
        .value_kind:     global_buffer
      - .actual_access:  read_only
        .address_space:  global
        .offset:         56
        .size:           8
        .value_kind:     global_buffer
      - .actual_access:  read_only
        .address_space:  global
        .offset:         64
        .size:           8
        .value_kind:     global_buffer
      - .actual_access:  write_only
        .address_space:  global
        .offset:         72
        .size:           8
        .value_kind:     global_buffer
      - .actual_access:  read_only
        .address_space:  global
        .offset:         80
        .size:           8
        .value_kind:     global_buffer
      - .actual_access:  read_only
        .address_space:  global
        .offset:         88
        .size:           8
        .value_kind:     global_buffer
    .group_segment_fixed_size: 0
    .kernarg_segment_align: 8
    .kernarg_segment_size: 96
    .language:       OpenCL C
    .language_version:
      - 2
      - 0
    .max_flat_workgroup_size: 1024
    .name:           _Z12layer_kernelILb0ELi0EEvPKfPKDF16_PKhS3_PK15HIP_vector_typeIiLj4EEPKtPKiS3_S1_PvPhPDF16_
    .private_segment_fixed_size: 0
    .sgpr_count:     70
    .sgpr_spill_count: 0
    .symbol:         _Z12layer_kernelILb0ELi0EEvPKfPKDF16_PKhS3_PK15HIP_vector_typeIiLj4EEPKtPKiS3_S1_PvPhPDF16_.kd
    .uniform_work_group_size: 1
    .uses_dynamic_stack: false
    .vgpr_count:     128
    .vgpr_spill_count: 0
    .wavefront_size: 64
